# w_e1, w_e2 and w_e2-tail conversion loops: global loads, counted vmcnt(16) per tile
# speedup vs baseline: 1.0082x; 1.0019x over previous
; #define LAS __attribute__((address_space(3)))
; #define TB_LOAD(R_, t_) do { const int _t = (t_); if (_t < tot) { const int _b = _t / per, _r = _t % per; ttb_load(R_, src + (size_t)_b * K_ * N_, N_, (_r % kt) * 128, (_r / kt) * 64, C.tid); } } while (0)
; __device__ __forceinline__ void ttb_load(TReg& R, const float* src, int ld, int k0, int n0, int tid) {
;     const int kr = tid >> 4, nq = tid & 15;
; #pragma unroll
;     for (int rep = 0; rep < 4; ++rep) R.v[rep] = __builtin_nontemporal_load((const f32x4*)(src + (size_t)(k0 + 4 * kr + rep) * ld + n0 + 4 * nq)); }
; __device__ __forceinline__ void ttb_put(const TReg& R, LAS unsigned* tile, int tid) {
;     const int kr = tid >> 4, nq = tid & 15;
; #pragma unroll
;     for (int c = 0; c < 4; ++c) { const int n = 4 * nq + c;
;         tile[n * 32 + (kr ^ (n & 31))] = pk4_fp8(R.v[0][c] * W_FP8_SCALE, R.v[1][c] * W_FP8_SCALE, R.v[2][c] * W_FP8_SCALE, R.v[3][c] * W_FP8_SCALE); } }
; __device__ __forceinline__ void ttb_finish(LAS const unsigned* tile, unsigned char* dst, int ldd, int k0, int n0, int map, int tid) {
;     const int n = tid >> 3, kq = tid & 7, m = n & 31, ns = n0 + n; int r = ns;
;     if (map == 2) { const int j = ns >> 1, par = ns & 1; r = 256 * (j >> 7) + 128 * par + (j & 127); }
;     const u32x4 g = *(LAS const u32x4*)(tile + n * 32 + 4 * (kq ^ (m >> 2)));
;     const unsigned a0 = (m & 1) ? g.y : g.x, a1 = (m & 1) ? g.x : g.y, a2 = (m & 1) ? g.w : g.z, a3 = (m & 1) ? g.z : g.w;
;     u32x4 w; w.x = (m & 2) ? a2 : a0; w.y = (m & 2) ? a3 : a1; w.z = (m & 2) ? a0 : a2; w.w = (m & 2) ? a1 : a3;
;     __builtin_nontemporal_store(w, (u32x4*)(dst + (size_t)r * ldd + k0 + 16 * kq));
; }
; template <int K_, int N_, int MAP_> __device__ __forceinline__ void tjob_b(const Ctx& C, int bid, int G, const float* src, unsigned char* dstb, int nbatch) {
;     constexpr int kt = K_ / 128, ntile = N_ / 64, per = kt * ntile; const int tot = per * nbatch;
;     TReg R0, R1, R2, R3; int kbuf = 0;
;     ...
;     TB_LOAD(R0, bid); TB_LOAD(R1, bid + G); TB_LOAD(R2, bid + 2 * G); TB_LOAD(R3, bid + 3 * G);
.LBB0_202:
	s_waitcnt vmcnt(0) lgkmcnt(0)
	v_mov_b64_e32 v[2:3], s[70:71]
	s_barrier
	flat_load_dwordx2 v[66:67], v[2:3] offset:200
	s_movk_i32 s8, 0x4000
	s_and_b64 s[6:7], s[2:3], exec
	s_cselect_b32 s25, s8, 0x2a00
	s_cmp_lt_i32 s1, s25
	s_cselect_b64 s[6:7], -1, 0
	s_cmp_ge_i32 s1, s25
	s_cbranch_scc1 .LBB0_204
	s_ashr_i32 s8, s1, 31
	s_lshr_b32 s8, s8, 23
	s_add_i32 s9, s1, s8
	s_ashr_i32 s8, s9, 9
	s_and_b32 s9, s9, 0xfe00
	s_sub_i32 s12, s1, s9
	s_sext_i32_i16 s13, s12
	s_bfe_u32 s13, s13, 0x4001b
	s_add_i32 s13, s12, s13
	s_sext_i32_i16 s26, s13
	s_and_b32 s13, s13, 0xfff0
	s_sub_i32 s12, s12, s13
	s_ashr_i32 s9, s8, 31
	s_sext_i32_i16 s27, s12
	s_lshl_b32 s12, s26, 2
	s_lshl_b64 s[8:9], s[8:9], 24
	s_andn2_b32 s12, s12, 63
	v_and_b32_e32 v4, -4, v69
	s_ashr_i32 s13, s12, 31
	s_waitcnt vmcnt(0) lgkmcnt(0)
	v_lshl_add_u64 v[2:3], v[66:67], 0, s[8:9]
	v_lshl_add_u32 v10, s27, 7, v4
	v_lshl_add_u64 v[2:3], s[12:13], 2, v[2:3]
	v_and_b32_e32 v4, 0xf0, v74
	v_mov_b32_e32 v5, 0
	v_ashrrev_i32_e32 v11, 31, v10
	v_lshl_add_u64 v[12:13], v[2:3], 0, v[4:5]
	v_lshlrev_b64 v[2:3], 13, v[10:11]
	v_lshl_add_u64 v[14:15], v[12:13], 0, v[2:3]
	v_or_b32_e32 v2, 1, v10
	v_ashrrev_i32_e32 v3, 31, v2
	v_lshlrev_b64 v[2:3], 13, v[2:3]
	v_lshl_add_u64 v[16:17], v[12:13], 0, v[2:3]
	global_load_dwordx4 v[2:5], v[14:15], off nt
	global_load_dwordx4 v[6:9], v[16:17], off nt
	v_or_b32_e32 v14, 2, v10
	v_ashrrev_i32_e32 v15, 31, v14
	v_or_b32_e32 v10, 3, v10
	v_lshlrev_b64 v[14:15], 13, v[14:15]
	v_ashrrev_i32_e32 v11, 31, v10
	v_lshl_add_u64 v[18:19], v[12:13], 0, v[14:15]
	v_lshlrev_b64 v[10:11], 13, v[10:11]
	v_lshl_add_u64 v[20:21], v[12:13], 0, v[10:11]
	global_load_dwordx4 v[10:13], v[18:19], off nt
	global_load_dwordx4 v[14:17], v[20:21], off nt
.LBB0_204:
	s_cmp_ge_i32 s22, s25
	s_cbranch_scc1 .LBB0_206
	s_ashr_i32 s8, s22, 31
	s_lshr_b32 s8, s8, 23
	s_add_i32 s9, s22, s8
	s_ashr_i32 s8, s9, 9
	s_and_b32 s9, s9, 0xfe00
	s_sub_i32 s12, s22, s9
	s_sext_i32_i16 s13, s12
	s_bfe_u32 s13, s13, 0x4001b
	s_add_i32 s13, s12, s13
	s_sext_i32_i16 s22, s13
	s_and_b32 s13, s13, 0xfff0
	s_sub_i32 s12, s12, s13
	s_ashr_i32 s9, s8, 31
	s_sext_i32_i16 s26, s12
	s_lshl_b32 s12, s22, 2
	s_lshl_b64 s[8:9], s[8:9], 24
	s_andn2_b32 s12, s12, 63
	v_and_b32_e32 v20, -4, v69
	s_ashr_i32 s13, s12, 31
	s_waitcnt vmcnt(0) lgkmcnt(0)
	v_lshl_add_u64 v[18:19], v[66:67], 0, s[8:9]
	v_lshl_add_u32 v26, s26, 7, v20
	v_lshl_add_u64 v[18:19], s[12:13], 2, v[18:19]
	v_and_b32_e32 v20, 0xf0, v74
	v_mov_b32_e32 v21, 0
	v_ashrrev_i32_e32 v27, 31, v26
	v_lshl_add_u64 v[28:29], v[18:19], 0, v[20:21]
	v_lshlrev_b64 v[18:19], 13, v[26:27]
	v_lshl_add_u64 v[30:31], v[28:29], 0, v[18:19]
	v_or_b32_e32 v18, 1, v26
	v_ashrrev_i32_e32 v19, 31, v18
	v_lshlrev_b64 v[18:19], 13, v[18:19]
	v_lshl_add_u64 v[32:33], v[28:29], 0, v[18:19]
	global_load_dwordx4 v[18:21], v[30:31], off nt
	global_load_dwordx4 v[22:25], v[32:33], off nt
	v_or_b32_e32 v30, 2, v26
	v_ashrrev_i32_e32 v31, 31, v30
	v_or_b32_e32 v26, 3, v26
	v_lshlrev_b64 v[30:31], 13, v[30:31]
	v_ashrrev_i32_e32 v27, 31, v26
	v_lshl_add_u64 v[34:35], v[28:29], 0, v[30:31]
	v_lshlrev_b64 v[26:27], 13, v[26:27]
	v_lshl_add_u64 v[36:37], v[28:29], 0, v[26:27]
	global_load_dwordx4 v[26:29], v[34:35], off nt
	global_load_dwordx4 v[30:33], v[36:37], off nt
.LBB0_206:
	s_cmp_ge_i32 s23, s25
	s_cbranch_scc1 .LBB0_208
	s_ashr_i32 s8, s23, 31
	s_lshr_b32 s8, s8, 23
	s_add_i32 s9, s23, s8
	s_ashr_i32 s8, s9, 9
	s_and_b32 s9, s9, 0xfe00
	s_sub_i32 s12, s23, s9
	s_sext_i32_i16 s13, s12
	s_bfe_u32 s13, s13, 0x4001b
	s_add_i32 s13, s12, s13
	s_sext_i32_i16 s22, s13
	s_and_b32 s13, s13, 0xfff0
	s_sub_i32 s12, s12, s13
	s_ashr_i32 s9, s8, 31
	s_sext_i32_i16 s23, s12
	s_lshl_b32 s12, s22, 2
	s_lshl_b64 s[8:9], s[8:9], 24
	s_andn2_b32 s12, s12, 63
	v_and_b32_e32 v36, -4, v69
	s_ashr_i32 s13, s12, 31
	s_waitcnt vmcnt(0) lgkmcnt(0)
	v_lshl_add_u64 v[34:35], v[66:67], 0, s[8:9]
	v_lshl_add_u32 v42, s23, 7, v36
	v_lshl_add_u64 v[34:35], s[12:13], 2, v[34:35]
	v_and_b32_e32 v36, 0xf0, v74
	v_mov_b32_e32 v37, 0
	v_ashrrev_i32_e32 v43, 31, v42
	v_lshl_add_u64 v[44:45], v[34:35], 0, v[36:37]
	v_lshlrev_b64 v[34:35], 13, v[42:43]
	v_lshl_add_u64 v[46:47], v[44:45], 0, v[34:35]
	v_or_b32_e32 v34, 1, v42
	v_ashrrev_i32_e32 v35, 31, v34
	v_lshlrev_b64 v[34:35], 13, v[34:35]
	v_lshl_add_u64 v[48:49], v[44:45], 0, v[34:35]
	global_load_dwordx4 v[34:37], v[46:47], off nt
	global_load_dwordx4 v[38:41], v[48:49], off nt
	v_or_b32_e32 v46, 2, v42
	v_ashrrev_i32_e32 v47, 31, v46
	v_or_b32_e32 v42, 3, v42
	v_lshlrev_b64 v[46:47], 13, v[46:47]
	v_ashrrev_i32_e32 v43, 31, v42
	v_lshl_add_u64 v[50:51], v[44:45], 0, v[46:47]
	v_lshlrev_b64 v[42:43], 13, v[42:43]
	v_lshl_add_u64 v[52:53], v[44:45], 0, v[42:43]
	global_load_dwordx4 v[42:45], v[50:51], off nt
	global_load_dwordx4 v[46:49], v[52:53], off nt
.LBB0_208:
	s_cmp_ge_i32 s24, s25
	s_cbranch_scc1 .LBB0_210
	s_ashr_i32 s8, s24, 31
	s_lshr_b32 s8, s8, 23
	s_add_i32 s9, s24, s8
	s_ashr_i32 s8, s9, 9
	s_and_b32 s9, s9, 0xfe00
	s_sub_i32 s12, s24, s9
	s_sext_i32_i16 s13, s12
	s_bfe_u32 s13, s13, 0x4001b
	s_add_i32 s13, s12, s13
	s_sext_i32_i16 s22, s13
	s_and_b32 s13, s13, 0xfff0
	s_sub_i32 s12, s12, s13
	s_ashr_i32 s9, s8, 31
	s_sext_i32_i16 s23, s12
	s_lshl_b32 s12, s22, 2
	s_lshl_b64 s[8:9], s[8:9], 24
	s_andn2_b32 s12, s12, 63
	v_and_b32_e32 v52, -4, v69
	s_ashr_i32 s13, s12, 31
	s_waitcnt vmcnt(0) lgkmcnt(0)
	v_lshl_add_u64 v[50:51], v[66:67], 0, s[8:9]
	v_lshl_add_u32 v58, s23, 7, v52
	v_lshl_add_u64 v[50:51], s[12:13], 2, v[50:51]
	v_and_b32_e32 v52, 0xf0, v74
	v_mov_b32_e32 v53, 0
	v_ashrrev_i32_e32 v59, 31, v58
	v_lshl_add_u64 v[60:61], v[50:51], 0, v[52:53]
	v_lshlrev_b64 v[50:51], 13, v[58:59]
	v_lshl_add_u64 v[62:63], v[60:61], 0, v[50:51]
	v_or_b32_e32 v50, 1, v58
	v_ashrrev_i32_e32 v51, 31, v50
	v_lshlrev_b64 v[50:51], 13, v[50:51]
	v_lshl_add_u64 v[64:65], v[60:61], 0, v[50:51]
	global_load_dwordx4 v[50:53], v[62:63], off nt
	global_load_dwordx4 v[54:57], v[64:65], off nt
	v_or_b32_e32 v62, 2, v58
	v_ashrrev_i32_e32 v63, 31, v62
	v_or_b32_e32 v58, 3, v58
	v_lshlrev_b64 v[62:63], 13, v[62:63]
	v_ashrrev_i32_e32 v59, 31, v58
	v_lshl_add_u64 v[70:71], v[60:61], 0, v[62:63]
	v_lshlrev_b64 v[58:59], 13, v[58:59]
	v_lshl_add_u64 v[72:73], v[60:61], 0, v[58:59]
	global_load_dwordx4 v[58:61], v[70:71], off nt
	global_load_dwordx4 v[62:65], v[72:73], off nt
	s_andn2_b64 vcc, exec, s[6:7]
	s_cbranch_vccnz .LBB0_227
	s_branch .LBB0_211

; #define LAS __attribute__((address_space(3)))
; #define TB_LOAD(R_, t_) do { const int _t = (t_); if (_t < tot) { const int _b = _t / per, _r = _t % per; ttb_load(R_, src + (size_t)_b * K_ * N_, N_, (_r % kt) * 128, (_r / kt) * 64, C.tid); } } while (0)
; #define TB_STEP(R_, t_) do { const int _u = (t_); if (_u < tot) { LAS unsigned* tile = (LAS unsigned*)(C.lds + kbuf * 8192); ttb_put(R_, tile, C.tid); TB_LOAD(R_, _u + 4 * G); __syncthreads(); \
;         { const int _b = _u / per, _r = _u % per; ttb_finish(tile, dstb + (size_t)_b * K_ * (MAP_ == 2 ? 4096 : N_), K_, (_r % kt) * 128, (_r / kt) * 64, MAP_, C.tid); } kbuf ^= 1; } } while (0)
; __device__ __forceinline__ void ttb_put(const TReg& R, LAS unsigned* tile, int tid) {
;     const int kr = tid >> 4, nq = tid & 15;
; #pragma unroll
;     for (int c = 0; c < 4; ++c) { const int n = 4 * nq + c;
;         tile[n * 32 + (kr ^ (n & 31))] = pk4_fp8(R.v[0][c] * W_FP8_SCALE, R.v[1][c] * W_FP8_SCALE, R.v[2][c] * W_FP8_SCALE, R.v[3][c] * W_FP8_SCALE); } }
; __device__ __forceinline__ void ttb_finish(LAS const unsigned* tile, unsigned char* dst, int ldd, int k0, int n0, int map, int tid) {
;     const int n = tid >> 3, kq = tid & 7, m = n & 31, ns = n0 + n; int r = ns;
;     if (map == 2) { const int j = ns >> 1, par = ns & 1; r = 256 * (j >> 7) + 128 * par + (j & 127); }
;     const u32x4 g = *(LAS const u32x4*)(tile + n * 32 + 4 * (kq ^ (m >> 2)));
;     const unsigned a0 = (m & 1) ? g.y : g.x, a1 = (m & 1) ? g.x : g.y, a2 = (m & 1) ? g.w : g.z, a3 = (m & 1) ? g.z : g.w;
;     u32x4 w; w.x = (m & 2) ? a2 : a0; w.y = (m & 2) ? a3 : a1; w.z = (m & 2) ? a0 : a2; w.w = (m & 2) ? a1 : a3;
;     __builtin_nontemporal_store(w, (u32x4*)(dst + (size_t)r * ldd + k0 + 16 * kq));
; }
; template <int K_, int N_, int MAP_> __device__ __forceinline__ void tjob_b(const Ctx& C, int bid, int G, const float* src, unsigned char* dstb, int nbatch) {
;     constexpr int kt = K_ / 128, ntile = N_ / 64, per = kt * ntile; const int tot = per * nbatch;
;     TReg R0, R1, R2, R3; int kbuf = 0;
;     ...
;     TB_LOAD(R0, bid); TB_LOAD(R1, bid + G); TB_LOAD(R2, bid + 2 * G); TB_LOAD(R3, bid + 3 * G);
;     for (int t = bid; t < tot; t += 4 * G) { TB_STEP(R0, t); TB_STEP(R1, t + G); TB_STEP(R2, t + 2 * G); TB_STEP(R3, t + 3 * G); }
.LBB0_211:
	v_and_b32_e32 v68, 60, v79
	v_or_b32_e32 v70, 1, v68
	v_bitop3_b32 v72, v79, v78, 28 bitop3:0x6c
	v_bitop3_b32 v82, v70, v78, 29 bitop3:0x6c
	v_lshlrev_b32_e32 v79, 7, v70
	v_or_b32_e32 v70, 2, v68
	v_bitop3_b32 v83, v70, v78, 30 bitop3:0x6c
	v_lshlrev_b32_e32 v80, 7, v70
	v_or_b32_e32 v70, 3, v68
	v_bitop3_b32 v84, v70, v78, 31 bitop3:0x6c
	v_lshlrev_b32_e32 v78, 7, v70
	v_lshlrev_b32_e32 v70, 2, v75
	s_add_u32 s22, s62, 0x29910000
	v_bitop3_b32 v85, v1, v70, 28 bitop3:0x6c
	v_mov_b32_e32 v73, 0
	s_addc_u32 s23, s63, 0
	v_lshlrev_b32_e32 v74, 7, v68
	v_lshlrev_b32_e32 v81, 7, v1
	s_mov_b32 s24, 0
	v_cmp_eq_u32_e64 s[6:7], 0, v76
	v_cmp_eq_u32_e64 s[8:9], 0, v77
	v_lshlrev_b32_e32 v70, 4, v75
	v_mov_b32_e32 v71, v73
	v_and_b32_e32 v69, -4, v69
	s_mov_b32 s26, 0xc3e00000
	v_mov_b32_e32 v75, 0x43e00000
	v_lshlrev_b32_e32 v76, 2, v72
	v_lshlrev_b32_e32 v77, 2, v82
	v_lshlrev_b32_e32 v82, 2, v83
	v_lshlrev_b32_e32 v83, 2, v84
	v_lshlrev_b32_e32 v84, 2, v85
	s_waitcnt vmcnt(0)
	s_branch .LBB0_214

; #define LAS __attribute__((address_space(3)))
; #define TB_LOAD(R_, t_) do { const int _t = (t_); if (_t < tot) { const int _b = _t / per, _r = _t % per; ttb_load(R_, src + (size_t)_b * K_ * N_, N_, (_r % kt) * 128, (_r / kt) * 64, C.tid); } } while (0)
; #define TB_STEP(R_, t_) do { const int _u = (t_); if (_u < tot) { LAS unsigned* tile = (LAS unsigned*)(C.lds + kbuf * 8192); ttb_put(R_, tile, C.tid); TB_LOAD(R_, _u + 4 * G); __syncthreads(); \
;         { const int _b = _u / per, _r = _u % per; ttb_finish(tile, dstb + (size_t)_b * K_ * (MAP_ == 2 ? 4096 : N_), K_, (_r % kt) * 128, (_r / kt) * 64, MAP_, C.tid); } kbuf ^= 1; } } while (0)
; __device__ __forceinline__ void ttb_put(const TReg& R, LAS unsigned* tile, int tid) {
;     const int kr = tid >> 4, nq = tid & 15;
; #pragma unroll
;     for (int c = 0; c < 4; ++c) { const int n = 4 * nq + c;
;         tile[n * 32 + (kr ^ (n & 31))] = pk4_fp8(R.v[0][c] * W_FP8_SCALE, R.v[1][c] * W_FP8_SCALE, R.v[2][c] * W_FP8_SCALE, R.v[3][c] * W_FP8_SCALE); } }
; __device__ __forceinline__ void ttb_finish(LAS const unsigned* tile, unsigned char* dst, int ldd, int k0, int n0, int map, int tid) {
;     const int n = tid >> 3, kq = tid & 7, m = n & 31, ns = n0 + n; int r = ns;
;     if (map == 2) { const int j = ns >> 1, par = ns & 1; r = 256 * (j >> 7) + 128 * par + (j & 127); }
;     const u32x4 g = *(LAS const u32x4*)(tile + n * 32 + 4 * (kq ^ (m >> 2)));
;     const unsigned a0 = (m & 1) ? g.y : g.x, a1 = (m & 1) ? g.x : g.y, a2 = (m & 1) ? g.w : g.z, a3 = (m & 1) ? g.z : g.w;
;     u32x4 w; w.x = (m & 2) ? a2 : a0; w.y = (m & 2) ? a3 : a1; w.z = (m & 2) ? a0 : a2; w.w = (m & 2) ? a1 : a3;
;     __builtin_nontemporal_store(w, (u32x4*)(dst + (size_t)r * ldd + k0 + 16 * kq));
; }
; template <int K_, int N_, int MAP_> __device__ __forceinline__ void tjob_b(const Ctx& C, int bid, int G, const float* src, unsigned char* dstb, int nbatch) {
;     constexpr int kt = K_ / 128, ntile = N_ / 64, per = kt * ntile; const int tot = per * nbatch;
;     TReg R0, R1, R2, R3; int kbuf = 0;
;     ...
;     TB_LOAD(R0, bid); TB_LOAD(R1, bid + G); TB_LOAD(R2, bid + 2 * G); TB_LOAD(R3, bid + 3 * G);
;     for (int t = bid; t < tot; t += 4 * G) { TB_STEP(R0, t); TB_STEP(R1, t + G); TB_STEP(R2, t + 2 * G); TB_STEP(R3, t + 3 * G); }
.LBB0_214:
	s_waitcnt vmcnt(16) lgkmcnt(0)
	s_add_i32 s84, s1, s15
	s_cmp_lt_i32 s84, s25
	s_cbranch_scc1 .Lcv_j2_0
	s_waitcnt vmcnt(0)
.Lcv_j2_0:
	v_mul_f32_e32 v72, 0x43800000, v2
	v_mul_f32_e32 v85, 0x43800000, v6
	v_med3_f32 v72, v72, s26, v75
	v_med3_f32 v85, v85, s26, v75
	v_cvt_pk_fp8_f32 v87, v72, v85
	v_mul_f32_e32 v86, 0x43800000, v10
	v_mul_f32_e32 v72, 0x43800000, v14
	v_med3_f32 v85, v86, s26, v75
	v_med3_f32 v72, v72, s26, v75
	v_cvt_pk_fp8_f32 v87, v85, v72 op_sel:[0,0,1]
	v_mul_f32_e32 v72, 0x43800000, v3
	v_mul_f32_e32 v85, 0x43800000, v7
	v_med3_f32 v72, v72, s26, v75
	v_med3_f32 v85, v85, s26, v75
	v_cvt_pk_fp8_f32 v88, v72, v85
	v_mul_f32_e32 v86, 0x43800000, v11
	v_mul_f32_e32 v72, 0x43800000, v15
	v_med3_f32 v85, v86, s26, v75
	v_med3_f32 v72, v72, s26, v75
	s_lshl_b32 s12, s24, 13
	v_cvt_pk_fp8_f32 v88, v85, v72 op_sel:[0,0,1]
	s_add_i32 s31, s12, 0
	v_add3_u32 v72, s31, v74, v76
	ds_write_b32 v72, v87
	v_add3_u32 v72, s31, v79, v77
	ds_write_b32 v72, v88
	v_mul_f32_e32 v72, 0x43800000, v4
	v_mul_f32_e32 v85, 0x43800000, v8
	v_med3_f32 v72, v72, s26, v75
	v_med3_f32 v85, v85, s26, v75
	v_cvt_pk_fp8_f32 v87, v72, v85
	v_mul_f32_e32 v86, 0x43800000, v12
	v_mul_f32_e32 v72, 0x43800000, v16
	v_med3_f32 v85, v86, s26, v75
	v_med3_f32 v72, v72, s26, v75
	v_cvt_pk_fp8_f32 v87, v85, v72 op_sel:[0,0,1]
	v_mul_f32_e32 v72, 0x43800000, v5
	v_mul_f32_e32 v85, 0x43800000, v9
	v_med3_f32 v72, v72, s26, v75
	v_med3_f32 v85, v85, s26, v75
	v_cvt_pk_fp8_f32 v88, v72, v85
	v_mul_f32_e32 v86, 0x43800000, v13
	v_mul_f32_e32 v72, 0x43800000, v17
	v_med3_f32 v85, v86, s26, v75
	v_med3_f32 v72, v72, s26, v75
	v_cvt_pk_fp8_f32 v88, v85, v72 op_sel:[0,0,1]
	s_add_i32 s27, s1, s16
	s_cmp_ge_i32 s27, s25
	v_add3_u32 v72, s31, v80, v82
	s_cselect_b64 s[12:13], -1, 0
	ds_write_b32 v72, v87
	v_add3_u32 v72, s31, v78, v83
	s_and_b64 vcc, exec, s[12:13]
	ds_write_b32 v72, v88
	s_cbranch_vccnz .LBB0_216
	s_ashr_i32 s33, s27, 31
	s_lshr_b32 s33, s33, 23
	s_add_i32 s33, s27, s33
	s_ashr_i32 s34, s33, 9
	s_and_b32 s33, s33, 0xfe00
	s_ashr_i32 s35, s34, 31
	s_sub_i32 s33, s27, s33
	s_lshl_b64 s[34:35], s[34:35], 24
	v_lshl_add_u64 v[2:3], v[66:67], 0, s[34:35]
	s_sext_i32_i16 s34, s33
	s_bfe_u32 s34, s34, 0x4001b
	s_add_i32 s34, s33, s34
	s_sext_i32_i16 s35, s34
	s_and_b32 s34, s34, 0xfff0
	s_sub_i32 s33, s33, s34
	s_lshl_b32 s34, s35, 2
	s_sext_i32_i16 s33, s33
	s_andn2_b32 s34, s34, 63
	v_lshl_add_u32 v10, s33, 7, v69
	s_ashr_i32 s35, s34, 31
	v_lshl_add_u64 v[2:3], s[34:35], 2, v[2:3]
	v_lshlrev_b32_e32 v72, 2, v68
	v_ashrrev_i32_e32 v11, 31, v10
	v_lshl_add_u64 v[12:13], v[2:3], 0, v[72:73]
	v_lshlrev_b64 v[2:3], 13, v[10:11]
	v_lshl_add_u64 v[14:15], v[12:13], 0, v[2:3]
	v_or_b32_e32 v2, 1, v10
	v_ashrrev_i32_e32 v3, 31, v2
	v_lshlrev_b64 v[2:3], 13, v[2:3]
	v_lshl_add_u64 v[16:17], v[12:13], 0, v[2:3]
	global_load_dwordx4 v[2:5], v[14:15], off nt
	global_load_dwordx4 v[6:9], v[16:17], off nt
	v_or_b32_e32 v14, 2, v10
	v_ashrrev_i32_e32 v15, 31, v14
	v_or_b32_e32 v10, 3, v10
	v_lshlrev_b64 v[14:15], 13, v[14:15]
	v_ashrrev_i32_e32 v11, 31, v10
	v_lshl_add_u64 v[86:87], v[12:13], 0, v[14:15]
	v_lshlrev_b64 v[10:11], 13, v[10:11]
	v_lshl_add_u64 v[88:89], v[12:13], 0, v[10:11]
	global_load_dwordx4 v[10:13], v[86:87], off nt
	global_load_dwordx4 v[14:17], v[88:89], off nt
; #define LAS __attribute__((address_space(3)))
; #define TB_LOAD(R_, t_) do { const int _t = (t_); if (_t < tot) { const int _b = _t / per, _r = _t % per; ttb_load(R_, src + (size_t)_b * K_ * N_, N_, (_r % kt) * 128, (_r / kt) * 64, C.tid); } } while (0)
; #define TB_STEP(R_, t_) do { const int _u = (t_); if (_u < tot) { LAS unsigned* tile = (LAS unsigned*)(C.lds + kbuf * 8192); ttb_put(R_, tile, C.tid); TB_LOAD(R_, _u + 4 * G); __syncthreads(); \
;         { const int _b = _u / per, _r = _u % per; ttb_finish(tile, dstb + (size_t)_b * K_ * (MAP_ == 2 ? 4096 : N_), K_, (_r % kt) * 128, (_r / kt) * 64, MAP_, C.tid); } kbuf ^= 1; } } while (0)
; __device__ __forceinline__ void ttb_put(const TReg& R, LAS unsigned* tile, int tid) {
;     const int kr = tid >> 4, nq = tid & 15;
; #pragma unroll
;     for (int c = 0; c < 4; ++c) { const int n = 4 * nq + c;
;         tile[n * 32 + (kr ^ (n & 31))] = pk4_fp8(R.v[0][c] * W_FP8_SCALE, R.v[1][c] * W_FP8_SCALE, R.v[2][c] * W_FP8_SCALE, R.v[3][c] * W_FP8_SCALE); } }
; __device__ __forceinline__ void ttb_finish(LAS const unsigned* tile, unsigned char* dst, int ldd, int k0, int n0, int map, int tid) {
;     const int n = tid >> 3, kq = tid & 7, m = n & 31, ns = n0 + n; int r = ns;
;     if (map == 2) { const int j = ns >> 1, par = ns & 1; r = 256 * (j >> 7) + 128 * par + (j & 127); }
;     const u32x4 g = *(LAS const u32x4*)(tile + n * 32 + 4 * (kq ^ (m >> 2)));
;     const unsigned a0 = (m & 1) ? g.y : g.x, a1 = (m & 1) ? g.x : g.y, a2 = (m & 1) ? g.w : g.z, a3 = (m & 1) ? g.z : g.w;
;     u32x4 w; w.x = (m & 2) ? a2 : a0; w.y = (m & 2) ? a3 : a1; w.z = (m & 2) ? a0 : a2; w.w = (m & 2) ? a1 : a3;
;     __builtin_nontemporal_store(w, (u32x4*)(dst + (size_t)r * ldd + k0 + 16 * kq));
; }
; template <int K_, int N_, int MAP_> __device__ __forceinline__ void tjob_b(const Ctx& C, int bid, int G, const float* src, unsigned char* dstb, int nbatch) {
;     constexpr int kt = K_ / 128, ntile = N_ / 64, per = kt * ntile; const int tot = per * nbatch;
;     TReg R0, R1, R2, R3; int kbuf = 0;
;     ...
;     TB_LOAD(R0, bid); TB_LOAD(R1, bid + G); TB_LOAD(R2, bid + 2 * G); TB_LOAD(R3, bid + 3 * G);
;     for (int t = bid; t < tot; t += 4 * G) { TB_STEP(R0, t); TB_STEP(R1, t + G); TB_STEP(R2, t + 2 * G); TB_STEP(R3, t + 3 * G); }
.LBB0_216:
	s_ashr_i32 s33, s1, 31
	s_lshr_b32 s33, s33, 23
	s_add_i32 s33, s1, s33
	s_ashr_i32 s34, s33, 9
	s_and_b32 s33, s33, 0xfe00
	s_ashr_i32 s35, s34, 31
	s_sub_i32 s33, s1, s33
	s_lshl_b64 s[34:35], s[34:35], 22
	s_add_u32 s34, s22, s34
	s_sext_i32_i16 s36, s33
	v_add3_u32 v72, s31, v81, v84
	s_waitcnt lgkmcnt(0)
	s_barrier
	s_addc_u32 s35, s23, s35
	s_bfe_u32 s36, s36, 0x4001b
	ds_read_b128 v[86:89], v72
	s_add_i32 s36, s33, s36
	s_sext_i32_i16 s37, s36
	s_lshl_b32 s31, s37, 2
	s_and_b32 s36, s36, 0xfff0
	s_andn2_b32 s31, s31, 63
	s_sub_i32 s33, s33, s36
	v_add_u32_e32 v90, s31, v1
	s_waitcnt lgkmcnt(0)
	v_cndmask_b32_e64 v72, v87, v86, s[6:7]
	v_cndmask_b32_e64 v91, v89, v88, s[6:7]
	s_sext_i32_i16 s33, s33
	v_cndmask_b32_e64 v85, v86, v87, s[6:7]
	v_cndmask_b32_e64 v89, v88, v89, s[6:7]
	v_cndmask_b32_e64 v86, v91, v72, s[8:9]
	v_cndmask_b32_e64 v88, v72, v91, s[8:9]
	v_ashrrev_i32_e32 v91, 31, v90
	s_lshl_b32 s36, s33, 7
	v_lshlrev_b64 v[90:91], 11, v[90:91]
	v_lshl_add_u64 v[90:91], s[34:35], 0, v[90:91]
	s_ashr_i32 s37, s36, 31
	v_lshl_add_u64 v[90:91], v[90:91], 0, s[36:37]
	s_xor_b32 s33, s24, 1
	s_add_i32 s31, s0, s1
	v_cndmask_b32_e64 v87, v89, v85, s[8:9]
	v_cndmask_b32_e64 v89, v85, v89, s[8:9]
	v_lshl_add_u64 v[90:91], v[90:91], 0, v[70:71]
	s_cmp_ge_i32 s31, s25
	global_store_dwordx4 v[90:91], v[86:89], off nt
	s_cbranch_scc1 .LBB0_220
	s_waitcnt vmcnt(16)
	s_add_i32 s84, s31, s15
	s_cmp_lt_i32 s84, s25
	s_cbranch_scc1 .Lcv_j2_1
	s_waitcnt vmcnt(0)
.Lcv_j2_1:
	v_mul_f32_e32 v72, 0x43800000, v18
	v_mul_f32_e32 v85, 0x43800000, v22
	v_med3_f32 v72, v72, s26, v75
	v_med3_f32 v85, v85, s26, v75
	v_cvt_pk_fp8_f32 v87, v72, v85
	v_mul_f32_e32 v86, 0x43800000, v26
	v_mul_f32_e32 v72, 0x43800000, v30
	v_med3_f32 v85, v86, s26, v75
	v_med3_f32 v72, v72, s26, v75
	v_cvt_pk_fp8_f32 v87, v85, v72 op_sel:[0,0,1]
	s_lshl_b32 s33, s33, 13
	s_add_i32 s33, s33, 0
	v_add3_u32 v72, s33, v74, v76
	ds_write_b32 v72, v87
	v_mul_f32_e32 v72, 0x43800000, v19
	v_mul_f32_e32 v85, 0x43800000, v23
	v_med3_f32 v72, v72, s26, v75
	v_med3_f32 v85, v85, s26, v75
	v_cvt_pk_fp8_f32 v87, v72, v85
	v_mul_f32_e32 v86, 0x43800000, v27
	v_mul_f32_e32 v72, 0x43800000, v31
	v_med3_f32 v85, v86, s26, v75
	v_med3_f32 v72, v72, s26, v75
	v_cvt_pk_fp8_f32 v87, v85, v72 op_sel:[0,0,1]
	v_mul_f32_e32 v72, 0x43800000, v20
	v_mul_f32_e32 v85, 0x43800000, v24
	v_med3_f32 v72, v72, s26, v75
	v_med3_f32 v85, v85, s26, v75
	v_cvt_pk_fp8_f32 v88, v72, v85
	v_mul_f32_e32 v86, 0x43800000, v28
	v_mul_f32_e32 v72, 0x43800000, v32
	v_med3_f32 v85, v86, s26, v75
	v_med3_f32 v72, v72, s26, v75
	v_cvt_pk_fp8_f32 v88, v85, v72 op_sel:[0,0,1]
	v_add3_u32 v72, s33, v79, v77
	ds_write_b32 v72, v87
	v_add3_u32 v72, s33, v80, v82
	ds_write_b32 v72, v88
	v_mul_f32_e32 v72, 0x43800000, v21
	v_mul_f32_e32 v85, 0x43800000, v25
	v_med3_f32 v72, v72, s26, v75
	v_med3_f32 v85, v85, s26, v75
	v_cvt_pk_fp8_f32 v87, v72, v85
	v_mul_f32_e32 v86, 0x43800000, v29
	v_mul_f32_e32 v72, 0x43800000, v33
	v_med3_f32 v85, v86, s26, v75
	v_med3_f32 v72, v72, s26, v75
	v_cvt_pk_fp8_f32 v87, v85, v72 op_sel:[0,0,1]
	s_add_i32 s34, s19, s1
	v_add3_u32 v72, s33, v78, v83
	s_cmp_ge_i32 s34, s25
	ds_write_b32 v72, v87
	s_cbranch_scc1 .LBB0_219
	s_ashr_i32 s35, s34, 31
	s_lshr_b32 s35, s35, 23
	s_add_i32 s35, s34, s35
	s_ashr_i32 s36, s35, 9
	s_and_b32 s35, s35, 0xfe00
	s_ashr_i32 s37, s36, 31
	s_sub_i32 s38, s34, s35
	s_lshl_b64 s[34:35], s[36:37], 24
	v_lshl_add_u64 v[18:19], v[66:67], 0, s[34:35]
	s_sext_i32_i16 s34, s38
	s_bfe_u32 s34, s34, 0x4001b
	s_add_i32 s34, s38, s34
	s_sext_i32_i16 s35, s34
	s_and_b32 s34, s34, 0xfff0
	s_sub_i32 s34, s38, s34
	s_sext_i32_i16 s36, s34
	s_lshl_b32 s34, s35, 2
	s_andn2_b32 s34, s34, 63
	v_lshl_add_u32 v26, s36, 7, v69
	s_ashr_i32 s35, s34, 31
	v_lshl_add_u64 v[18:19], s[34:35], 2, v[18:19]
	v_lshlrev_b32_e32 v72, 2, v68
	v_ashrrev_i32_e32 v27, 31, v26
	v_lshl_add_u64 v[28:29], v[18:19], 0, v[72:73]
	v_lshlrev_b64 v[18:19], 13, v[26:27]
	v_lshl_add_u64 v[30:31], v[28:29], 0, v[18:19]
	v_or_b32_e32 v18, 1, v26
	v_ashrrev_i32_e32 v19, 31, v18
	v_lshlrev_b64 v[18:19], 13, v[18:19]
	v_lshl_add_u64 v[32:33], v[28:29], 0, v[18:19]
	global_load_dwordx4 v[18:21], v[30:31], off nt
	global_load_dwordx4 v[22:25], v[32:33], off nt
	v_or_b32_e32 v30, 2, v26
	v_ashrrev_i32_e32 v31, 31, v30
	v_or_b32_e32 v26, 3, v26
	v_lshlrev_b64 v[30:31], 13, v[30:31]
	v_ashrrev_i32_e32 v27, 31, v26
	v_lshl_add_u64 v[86:87], v[28:29], 0, v[30:31]
	v_lshlrev_b64 v[26:27], 13, v[26:27]
	v_lshl_add_u64 v[88:89], v[28:29], 0, v[26:27]
	global_load_dwordx4 v[26:29], v[86:87], off nt
	global_load_dwordx4 v[30:33], v[88:89], off nt

; #define LAS __attribute__((address_space(3)))
; #define TB_LOAD(R_, t_) do { const int _t = (t_); if (_t < tot) { const int _b = _t / per, _r = _t % per; ttb_load(R_, src + (size_t)_b * K_ * N_, N_, (_r % kt) * 128, (_r / kt) * 64, C.tid); } } while (0)
; #define TB_STEP(R_, t_) do { const int _u = (t_); if (_u < tot) { LAS unsigned* tile = (LAS unsigned*)(C.lds + kbuf * 8192); ttb_put(R_, tile, C.tid); TB_LOAD(R_, _u + 4 * G); __syncthreads(); \
;         { const int _b = _u / per, _r = _u % per; ttb_finish(tile, dstb + (size_t)_b * K_ * (MAP_ == 2 ? 4096 : N_), K_, (_r % kt) * 128, (_r / kt) * 64, MAP_, C.tid); } kbuf ^= 1; } } while (0)
; __device__ __forceinline__ void ttb_put(const TReg& R, LAS unsigned* tile, int tid) {
;     const int kr = tid >> 4, nq = tid & 15;
; #pragma unroll
;     for (int c = 0; c < 4; ++c) { const int n = 4 * nq + c;
;         tile[n * 32 + (kr ^ (n & 31))] = pk4_fp8(R.v[0][c] * W_FP8_SCALE, R.v[1][c] * W_FP8_SCALE, R.v[2][c] * W_FP8_SCALE, R.v[3][c] * W_FP8_SCALE); } }
; __device__ __forceinline__ void ttb_finish(LAS const unsigned* tile, unsigned char* dst, int ldd, int k0, int n0, int map, int tid) {
;     const int n = tid >> 3, kq = tid & 7, m = n & 31, ns = n0 + n; int r = ns;
;     if (map == 2) { const int j = ns >> 1, par = ns & 1; r = 256 * (j >> 7) + 128 * par + (j & 127); }
;     const u32x4 g = *(LAS const u32x4*)(tile + n * 32 + 4 * (kq ^ (m >> 2)));
;     const unsigned a0 = (m & 1) ? g.y : g.x, a1 = (m & 1) ? g.x : g.y, a2 = (m & 1) ? g.w : g.z, a3 = (m & 1) ? g.z : g.w;
;     u32x4 w; w.x = (m & 2) ? a2 : a0; w.y = (m & 2) ? a3 : a1; w.z = (m & 2) ? a0 : a2; w.w = (m & 2) ? a1 : a3;
;     __builtin_nontemporal_store(w, (u32x4*)(dst + (size_t)r * ldd + k0 + 16 * kq));
; }
; template <int K_, int N_, int MAP_> __device__ __forceinline__ void tjob_b(const Ctx& C, int bid, int G, const float* src, unsigned char* dstb, int nbatch) {
;     constexpr int kt = K_ / 128, ntile = N_ / 64, per = kt * ntile; const int tot = per * nbatch;
;     TReg R0, R1, R2, R3; int kbuf = 0;
;     ...
;     TB_LOAD(R0, bid); TB_LOAD(R1, bid + G); TB_LOAD(R2, bid + 2 * G); TB_LOAD(R3, bid + 3 * G);
;     for (int t = bid; t < tot; t += 4 * G) { TB_STEP(R0, t); TB_STEP(R1, t + G); TB_STEP(R2, t + 2 * G); TB_STEP(R3, t + 3 * G); }
.LBB0_221:
	s_waitcnt vmcnt(16)
	s_add_i32 s84, s31, s15
	s_cmp_lt_i32 s84, s25
	s_cbranch_scc1 .Lcv_j2_2
	s_waitcnt vmcnt(0)
.Lcv_j2_2:
	v_mul_f32_e32 v72, 0x43800000, v34
	v_mul_f32_e32 v85, 0x43800000, v38
	v_med3_f32 v72, v72, s26, v75
	v_med3_f32 v85, v85, s26, v75
	v_cvt_pk_fp8_f32 v87, v72, v85
	v_mul_f32_e32 v86, 0x43800000, v42
	v_mul_f32_e32 v72, 0x43800000, v46
	v_med3_f32 v85, v86, s26, v75
	v_med3_f32 v72, v72, s26, v75
	v_cvt_pk_fp8_f32 v87, v85, v72 op_sel:[0,0,1]
	s_lshl_b32 s33, s24, 13
	s_add_i32 s33, s33, 0
	v_add3_u32 v72, s33, v74, v76
	ds_write_b32 v72, v87
	v_mul_f32_e32 v72, 0x43800000, v35
	v_mul_f32_e32 v85, 0x43800000, v39
	v_med3_f32 v72, v72, s26, v75
	v_med3_f32 v85, v85, s26, v75
	v_cvt_pk_fp8_f32 v87, v72, v85
	v_mul_f32_e32 v86, 0x43800000, v43
	v_mul_f32_e32 v72, 0x43800000, v47
	v_med3_f32 v85, v86, s26, v75
	v_med3_f32 v72, v72, s26, v75
	v_cvt_pk_fp8_f32 v87, v85, v72 op_sel:[0,0,1]
	v_mul_f32_e32 v72, 0x43800000, v36
	v_mul_f32_e32 v85, 0x43800000, v40
	v_med3_f32 v72, v72, s26, v75
	v_med3_f32 v85, v85, s26, v75
	v_cvt_pk_fp8_f32 v88, v72, v85
	v_mul_f32_e32 v86, 0x43800000, v44
	v_mul_f32_e32 v72, 0x43800000, v48
	v_med3_f32 v85, v86, s26, v75
	v_med3_f32 v72, v72, s26, v75
	v_cvt_pk_fp8_f32 v88, v85, v72 op_sel:[0,0,1]
	v_add3_u32 v72, s33, v79, v77
	ds_write_b32 v72, v87
	v_add3_u32 v72, s33, v80, v82
	ds_write_b32 v72, v88
	v_mul_f32_e32 v72, 0x43800000, v37
	v_mul_f32_e32 v85, 0x43800000, v41
	v_med3_f32 v72, v72, s26, v75
	v_med3_f32 v85, v85, s26, v75
	v_cvt_pk_fp8_f32 v87, v72, v85
	v_mul_f32_e32 v86, 0x43800000, v45
	v_mul_f32_e32 v72, 0x43800000, v49
	v_med3_f32 v85, v86, s26, v75
	v_med3_f32 v72, v72, s26, v75
	v_cvt_pk_fp8_f32 v87, v85, v72 op_sel:[0,0,1]
	s_add_i32 s34, s18, s1
	v_add3_u32 v72, s33, v78, v83
	s_cmp_ge_i32 s34, s25
	ds_write_b32 v72, v87
	s_cbranch_scc1 .LBB0_223
	s_ashr_i32 s35, s34, 31
	s_lshr_b32 s35, s35, 23
	s_add_i32 s35, s34, s35
	s_ashr_i32 s36, s35, 9
	s_and_b32 s35, s35, 0xfe00
	s_ashr_i32 s37, s36, 31
	s_sub_i32 s38, s34, s35
	s_lshl_b64 s[34:35], s[36:37], 24
	v_lshl_add_u64 v[34:35], v[66:67], 0, s[34:35]
	s_sext_i32_i16 s34, s38
	s_bfe_u32 s34, s34, 0x4001b
	s_add_i32 s34, s38, s34
	s_sext_i32_i16 s35, s34
	s_and_b32 s34, s34, 0xfff0
	s_sub_i32 s34, s38, s34
	s_sext_i32_i16 s36, s34
	s_lshl_b32 s34, s35, 2
	s_andn2_b32 s34, s34, 63
	v_lshl_add_u32 v42, s36, 7, v69
	s_ashr_i32 s35, s34, 31
	v_lshl_add_u64 v[34:35], s[34:35], 2, v[34:35]
	v_lshlrev_b32_e32 v72, 2, v68
	v_ashrrev_i32_e32 v43, 31, v42
	v_lshl_add_u64 v[44:45], v[34:35], 0, v[72:73]
	v_lshlrev_b64 v[34:35], 13, v[42:43]
	v_lshl_add_u64 v[46:47], v[44:45], 0, v[34:35]
	v_or_b32_e32 v34, 1, v42
	v_ashrrev_i32_e32 v35, 31, v34
	v_lshlrev_b64 v[34:35], 13, v[34:35]
	v_lshl_add_u64 v[48:49], v[44:45], 0, v[34:35]
	global_load_dwordx4 v[34:37], v[46:47], off nt
	global_load_dwordx4 v[38:41], v[48:49], off nt
	v_or_b32_e32 v46, 2, v42
	v_ashrrev_i32_e32 v47, 31, v46
	v_or_b32_e32 v42, 3, v42
	v_lshlrev_b64 v[46:47], 13, v[46:47]
	v_ashrrev_i32_e32 v43, 31, v42
	v_lshl_add_u64 v[86:87], v[44:45], 0, v[46:47]
	v_lshlrev_b64 v[42:43], 13, v[42:43]
	v_lshl_add_u64 v[88:89], v[44:45], 0, v[42:43]
	global_load_dwordx4 v[42:45], v[86:87], off nt
	global_load_dwordx4 v[46:49], v[88:89], off nt

; #define LAS __attribute__((address_space(3)))
; #define TB_LOAD(R_, t_) do { const int _t = (t_); if (_t < tot) { const int _b = _t / per, _r = _t % per; ttb_load(R_, src + (size_t)_b * K_ * N_, N_, (_r % kt) * 128, (_r / kt) * 64, C.tid); } } while (0)
; #define TB_STEP(R_, t_) do { const int _u = (t_); if (_u < tot) { LAS unsigned* tile = (LAS unsigned*)(C.lds + kbuf * 8192); ttb_put(R_, tile, C.tid); TB_LOAD(R_, _u + 4 * G); __syncthreads(); \
;         { const int _b = _u / per, _r = _u % per; ttb_finish(tile, dstb + (size_t)_b * K_ * (MAP_ == 2 ? 4096 : N_), K_, (_r % kt) * 128, (_r / kt) * 64, MAP_, C.tid); } kbuf ^= 1; } } while (0)
; __device__ __forceinline__ void ttb_put(const TReg& R, LAS unsigned* tile, int tid) {
;     const int kr = tid >> 4, nq = tid & 15;
; #pragma unroll
;     for (int c = 0; c < 4; ++c) { const int n = 4 * nq + c;
;         tile[n * 32 + (kr ^ (n & 31))] = pk4_fp8(R.v[0][c] * W_FP8_SCALE, R.v[1][c] * W_FP8_SCALE, R.v[2][c] * W_FP8_SCALE, R.v[3][c] * W_FP8_SCALE); } }
; __device__ __forceinline__ void ttb_finish(LAS const unsigned* tile, unsigned char* dst, int ldd, int k0, int n0, int map, int tid) {
;     const int n = tid >> 3, kq = tid & 7, m = n & 31, ns = n0 + n; int r = ns;
;     if (map == 2) { const int j = ns >> 1, par = ns & 1; r = 256 * (j >> 7) + 128 * par + (j & 127); }
;     const u32x4 g = *(LAS const u32x4*)(tile + n * 32 + 4 * (kq ^ (m >> 2)));
;     const unsigned a0 = (m & 1) ? g.y : g.x, a1 = (m & 1) ? g.x : g.y, a2 = (m & 1) ? g.w : g.z, a3 = (m & 1) ? g.z : g.w;
;     u32x4 w; w.x = (m & 2) ? a2 : a0; w.y = (m & 2) ? a3 : a1; w.z = (m & 2) ? a0 : a2; w.w = (m & 2) ? a1 : a3;
;     __builtin_nontemporal_store(w, (u32x4*)(dst + (size_t)r * ldd + k0 + 16 * kq));
; }
; template <int K_, int N_, int MAP_> __device__ __forceinline__ void tjob_b(const Ctx& C, int bid, int G, const float* src, unsigned char* dstb, int nbatch) {
;     constexpr int kt = K_ / 128, ntile = N_ / 64, per = kt * ntile; const int tot = per * nbatch;
;     TReg R0, R1, R2, R3; int kbuf = 0;
;     ...
;     TB_LOAD(R0, bid); TB_LOAD(R1, bid + G); TB_LOAD(R2, bid + 2 * G); TB_LOAD(R3, bid + 3 * G);
;     for (int t = bid; t < tot; t += 4 * G) { TB_STEP(R0, t); TB_STEP(R1, t + G); TB_STEP(R2, t + 2 * G); TB_STEP(R3, t + 3 * G); }
.LBB0_224:
	s_add_i32 s31, s15, s1
	s_cmp_ge_i32 s31, s25
	s_cbranch_scc1 .LBB0_213
	s_waitcnt vmcnt(16)
	s_add_i32 s84, s31, s15
	s_cmp_lt_i32 s84, s25
	s_cbranch_scc1 .Lcv_j2_3
	s_waitcnt vmcnt(0)
.Lcv_j2_3:
	v_mul_f32_e32 v72, 0x43800000, v50
	v_mul_f32_e32 v85, 0x43800000, v54
	v_med3_f32 v72, v72, s26, v75
	v_med3_f32 v85, v85, s26, v75
	v_cvt_pk_fp8_f32 v87, v72, v85
	v_mul_f32_e32 v86, 0x43800000, v58
	v_mul_f32_e32 v72, 0x43800000, v62
	v_med3_f32 v85, v86, s26, v75
	v_med3_f32 v72, v72, s26, v75
	v_cvt_pk_fp8_f32 v87, v85, v72 op_sel:[0,0,1]
	s_lshl_b32 s33, s24, 13
	s_add_i32 s33, s33, 0
	v_add3_u32 v72, s33, v74, v76
	ds_write_b32 v72, v87
	v_mul_f32_e32 v72, 0x43800000, v51
	v_mul_f32_e32 v85, 0x43800000, v55
	v_med3_f32 v72, v72, s26, v75
	v_med3_f32 v85, v85, s26, v75
	v_cvt_pk_fp8_f32 v87, v72, v85
	v_mul_f32_e32 v86, 0x43800000, v59
	v_mul_f32_e32 v72, 0x43800000, v63
	v_med3_f32 v85, v86, s26, v75
	v_med3_f32 v72, v72, s26, v75
	v_cvt_pk_fp8_f32 v87, v85, v72 op_sel:[0,0,1]
	v_mul_f32_e32 v72, 0x43800000, v52
	v_mul_f32_e32 v85, 0x43800000, v56
	v_med3_f32 v72, v72, s26, v75
	v_med3_f32 v85, v85, s26, v75
	v_cvt_pk_fp8_f32 v88, v72, v85
	v_mul_f32_e32 v86, 0x43800000, v60
	v_mul_f32_e32 v72, 0x43800000, v64
	v_med3_f32 v85, v86, s26, v75
	v_med3_f32 v72, v72, s26, v75
	v_cvt_pk_fp8_f32 v88, v85, v72 op_sel:[0,0,1]
	v_add3_u32 v72, s33, v79, v77
	ds_write_b32 v72, v87
	v_add3_u32 v72, s33, v80, v82
	ds_write_b32 v72, v88
	v_mul_f32_e32 v72, 0x43800000, v53
	v_mul_f32_e32 v85, 0x43800000, v57
	v_med3_f32 v72, v72, s26, v75
	v_med3_f32 v85, v85, s26, v75
	v_cvt_pk_fp8_f32 v87, v72, v85
	v_mul_f32_e32 v86, 0x43800000, v61
	v_mul_f32_e32 v72, 0x43800000, v65
	v_med3_f32 v85, v86, s26, v75
	v_med3_f32 v72, v72, s26, v75
	v_cvt_pk_fp8_f32 v87, v85, v72 op_sel:[0,0,1]
	s_add_i32 s1, s17, s1
	v_add3_u32 v72, s33, v78, v83
	s_cmp_ge_i32 s1, s25
	ds_write_b32 v72, v87
	s_cbranch_scc1 .LBB0_212
	s_ashr_i32 s34, s1, 31
	s_lshr_b32 s34, s34, 23
	s_add_i32 s35, s1, s34
	s_ashr_i32 s34, s35, 9
	s_and_b32 s35, s35, 0xfe00
	s_sub_i32 s1, s1, s35
	s_ashr_i32 s35, s34, 31
	s_lshl_b64 s[34:35], s[34:35], 24
	v_lshl_add_u64 v[50:51], v[66:67], 0, s[34:35]
	s_sext_i32_i16 s34, s1
	s_bfe_u32 s34, s34, 0x4001b
	s_add_i32 s34, s1, s34
	s_sext_i32_i16 s35, s34
	s_and_b32 s34, s34, 0xfff0
	s_sub_i32 s1, s1, s34
	s_lshl_b32 s34, s35, 2
	s_sext_i32_i16 s1, s1
	s_andn2_b32 s34, s34, 63
	v_lshl_add_u32 v58, s1, 7, v69
	s_ashr_i32 s35, s34, 31
	v_lshl_add_u64 v[50:51], s[34:35], 2, v[50:51]
	v_lshlrev_b32_e32 v72, 2, v68
	v_ashrrev_i32_e32 v59, 31, v58
	v_lshl_add_u64 v[60:61], v[50:51], 0, v[72:73]
	v_lshlrev_b64 v[50:51], 13, v[58:59]
	v_lshl_add_u64 v[62:63], v[60:61], 0, v[50:51]
	v_or_b32_e32 v50, 1, v58
	v_ashrrev_i32_e32 v51, 31, v50
	v_lshlrev_b64 v[50:51], 13, v[50:51]
	v_lshl_add_u64 v[64:65], v[60:61], 0, v[50:51]
	global_load_dwordx4 v[50:53], v[62:63], off nt
	global_load_dwordx4 v[54:57], v[64:65], off nt
	v_or_b32_e32 v62, 2, v58
	v_ashrrev_i32_e32 v63, 31, v62
	v_or_b32_e32 v58, 3, v58
	v_lshlrev_b64 v[62:63], 13, v[62:63]
	v_ashrrev_i32_e32 v59, 31, v58
	v_lshl_add_u64 v[86:87], v[60:61], 0, v[62:63]
	v_lshlrev_b64 v[58:59], 13, v[58:59]
	v_lshl_add_u64 v[88:89], v[60:61], 0, v[58:59]
	global_load_dwordx4 v[58:61], v[86:87], off nt
	global_load_dwordx4 v[62:65], v[88:89], off nt
	s_branch .LBB0_212

; #define LAS __attribute__((address_space(3)))
; #define TB_LOAD(R_, t_) do { const int _t = (t_); if (_t < tot) { const int _b = _t / per, _r = _t % per; ttb_load(R_, src + (size_t)_b * K_ * N_, N_, (_r % kt) * 128, (_r / kt) * 64, C.tid); } } while (0)
; __device__ __forceinline__ void ttb_load(TReg& R, const float* src, int ld, int k0, int n0, int tid) {
;     const int kr = tid >> 4, nq = tid & 15;
; #pragma unroll
;     for (int rep = 0; rep < 4; ++rep) R.v[rep] = __builtin_nontemporal_load((const f32x4*)(src + (size_t)(k0 + 4 * kr + rep) * ld + n0 + 4 * nq)); }
; __device__ __forceinline__ void ttb_put(const TReg& R, LAS unsigned* tile, int tid) {
;     const int kr = tid >> 4, nq = tid & 15;
; #pragma unroll
;     for (int c = 0; c < 4; ++c) { const int n = 4 * nq + c;
;         tile[n * 32 + (kr ^ (n & 31))] = pk4_fp8(R.v[0][c] * W_FP8_SCALE, R.v[1][c] * W_FP8_SCALE, R.v[2][c] * W_FP8_SCALE, R.v[3][c] * W_FP8_SCALE); } }
; __device__ __forceinline__ void ttb_finish(LAS const unsigned* tile, unsigned char* dst, int ldd, int k0, int n0, int map, int tid) {
;     const int n = tid >> 3, kq = tid & 7, m = n & 31, ns = n0 + n; int r = ns;
;     if (map == 2) { const int j = ns >> 1, par = ns & 1; r = 256 * (j >> 7) + 128 * par + (j & 127); }
;     const u32x4 g = *(LAS const u32x4*)(tile + n * 32 + 4 * (kq ^ (m >> 2)));
;     const unsigned a0 = (m & 1) ? g.y : g.x, a1 = (m & 1) ? g.x : g.y, a2 = (m & 1) ? g.w : g.z, a3 = (m & 1) ? g.z : g.w;
;     u32x4 w; w.x = (m & 2) ? a2 : a0; w.y = (m & 2) ? a3 : a1; w.z = (m & 2) ? a0 : a2; w.w = (m & 2) ? a1 : a3;
;     __builtin_nontemporal_store(w, (u32x4*)(dst + (size_t)r * ldd + k0 + 16 * kq));
; }
; template <int K_, int N_, int MAP_> __device__ __forceinline__ void tjob_b(const Ctx& C, int bid, int G, const float* src, unsigned char* dstb, int nbatch) {
;     constexpr int kt = K_ / 128, ntile = N_ / 64, per = kt * ntile; const int tot = per * nbatch;
;     TReg R0, R1, R2, R3; int kbuf = 0;
;     ...
;     TB_LOAD(R0, bid); TB_LOAD(R1, bid + G); TB_LOAD(R2, bid + 2 * G); TB_LOAD(R3, bid + 3 * G);
.LBB0_269:
	v_mov_b32_e32 v70, v0
	s_andn2_b64 vcc, exec, s[20:21]
	s_mov_b64 s[0:1], s[70:71]
	s_cbranch_vccnz .LBB0_278
	v_mov_b64_e32 v[2:3], s[0:1]
	flat_load_dwordx2 v[2:3], v[2:3] offset:200
	v_readlane_b32 s10, v254, 0
	s_mov_b64 s[70:71], s[0:1]
	s_cmpk_lt_i32 s10, 0x1600
	s_mov_b64 s[0:1], 0x15000000
	v_ashrrev_i32_e32 v72, 2, v70
	s_cselect_b64 s[2:3], -1, 0
	s_cmpk_gt_i32 s10, 0x15ff
	v_lshlrev_b32_e32 v1, 4, v70
	v_readlane_b32 s11, v254, 1
	s_waitcnt vmcnt(0) lgkmcnt(0)
	v_lshl_add_u64 v[66:67], v[2:3], 0, s[0:1]
	s_cbranch_scc1 .LBB0_272
	s_ashr_i32 s0, s10, 31
	s_lshr_b32 s0, s0, 23
	s_add_i32 s1, s10, s0
	s_ashr_i32 s0, s1, 9
	s_and_b32 s1, s1, 0xfe00
	s_sub_i32 s6, s10, s1
	s_sext_i32_i16 s7, s6
	s_bfe_u32 s7, s7, 0x4001b
	s_add_i32 s7, s6, s7
	s_sext_i32_i16 s8, s7
	s_and_b32 s7, s7, 0xfff0
	s_sub_i32 s6, s6, s7
	s_ashr_i32 s1, s0, 31
	s_sext_i32_i16 s9, s6
	s_lshl_b32 s6, s8, 2
	s_lshl_b64 s[0:1], s[0:1], 24
	s_andn2_b32 s6, s6, 63
	v_and_b32_e32 v4, -4, v72
	s_ashr_i32 s7, s6, 31
	v_lshl_add_u64 v[2:3], v[66:67], 0, s[0:1]
	v_lshl_add_u32 v10, s9, 7, v4
	v_lshl_add_u64 v[2:3], s[6:7], 2, v[2:3]
	v_and_b32_e32 v4, 0xf0, v1
	v_mov_b32_e32 v5, 0
	v_ashrrev_i32_e32 v11, 31, v10
	v_lshl_add_u64 v[12:13], v[2:3], 0, v[4:5]
	v_lshlrev_b64 v[2:3], 13, v[10:11]
	v_lshl_add_u64 v[14:15], v[12:13], 0, v[2:3]
	v_or_b32_e32 v2, 1, v10
	v_ashrrev_i32_e32 v3, 31, v2
	v_lshlrev_b64 v[2:3], 13, v[2:3]
	v_lshl_add_u64 v[16:17], v[12:13], 0, v[2:3]
	global_load_dwordx4 v[2:5], v[14:15], off nt
	global_load_dwordx4 v[6:9], v[16:17], off nt
	v_or_b32_e32 v14, 2, v10
	v_ashrrev_i32_e32 v15, 31, v14
	v_or_b32_e32 v10, 3, v10
	v_lshlrev_b64 v[14:15], 13, v[14:15]
	v_ashrrev_i32_e32 v11, 31, v10
	v_lshl_add_u64 v[18:19], v[12:13], 0, v[14:15]
	v_lshlrev_b64 v[10:11], 13, v[10:11]
	v_lshl_add_u64 v[20:21], v[12:13], 0, v[10:11]
	global_load_dwordx4 v[10:13], v[18:19], off nt
	global_load_dwordx4 v[14:17], v[20:21], off nt
.LBB0_272:
	s_add_i32 s0, s28, s10
	s_cmpk_gt_i32 s0, 0x15ff
	s_cbranch_scc1 .LBB0_274
	s_ashr_i32 s1, s0, 31
	s_lshr_b32 s1, s1, 23
	s_add_i32 s1, s0, s1
	s_ashr_i32 s6, s1, 9
	s_and_b32 s1, s1, 0xfe00
	s_sub_i32 s1, s0, s1
	s_sext_i32_i16 s8, s1
	s_bfe_u32 s8, s8, 0x4001b
	s_add_i32 s8, s1, s8
	s_sext_i32_i16 s9, s8
	s_and_b32 s8, s8, 0xfff0
	s_ashr_i32 s7, s6, 31
	s_sub_i32 s1, s1, s8
	s_lshl_b32 s8, s9, 2
	s_lshl_b64 s[6:7], s[6:7], 24
	s_sext_i32_i16 s1, s1
	s_andn2_b32 s8, s8, 63
	v_and_b32_e32 v20, -4, v72
	s_ashr_i32 s9, s8, 31
	v_lshl_add_u64 v[18:19], v[66:67], 0, s[6:7]
	v_lshl_add_u32 v26, s1, 7, v20
	v_lshl_add_u64 v[18:19], s[8:9], 2, v[18:19]
	v_and_b32_e32 v20, 0xf0, v1
	v_mov_b32_e32 v21, 0
	v_ashrrev_i32_e32 v27, 31, v26
	v_lshl_add_u64 v[28:29], v[18:19], 0, v[20:21]
	v_lshlrev_b64 v[18:19], 13, v[26:27]
	v_lshl_add_u64 v[30:31], v[28:29], 0, v[18:19]
	v_or_b32_e32 v18, 1, v26
	v_ashrrev_i32_e32 v19, 31, v18
	v_lshlrev_b64 v[18:19], 13, v[18:19]
	v_lshl_add_u64 v[32:33], v[28:29], 0, v[18:19]
	global_load_dwordx4 v[18:21], v[30:31], off nt
	global_load_dwordx4 v[22:25], v[32:33], off nt
	v_or_b32_e32 v30, 2, v26
	v_ashrrev_i32_e32 v31, 31, v30
	v_or_b32_e32 v26, 3, v26
	v_lshlrev_b64 v[30:31], 13, v[30:31]
	v_ashrrev_i32_e32 v27, 31, v26
	v_lshl_add_u64 v[34:35], v[28:29], 0, v[30:31]
	v_lshlrev_b64 v[26:27], 13, v[26:27]
	v_lshl_add_u64 v[36:37], v[28:29], 0, v[26:27]
	global_load_dwordx4 v[26:29], v[34:35], off nt
	global_load_dwordx4 v[30:33], v[36:37], off nt
.LBB0_274:
	s_add_i32 s0, s0, s28
	s_cmpk_gt_i32 s0, 0x15ff
	s_cbranch_scc1 .LBB0_276
	s_ashr_i32 s1, s0, 31
	s_lshr_b32 s1, s1, 23
	s_add_i32 s1, s0, s1
	s_ashr_i32 s6, s1, 9
	s_and_b32 s1, s1, 0xfe00
	s_sub_i32 s1, s0, s1
	s_sext_i32_i16 s8, s1
	s_bfe_u32 s8, s8, 0x4001b
	s_add_i32 s8, s1, s8
	s_sext_i32_i16 s9, s8
	s_and_b32 s8, s8, 0xfff0
	s_ashr_i32 s7, s6, 31
	s_sub_i32 s1, s1, s8
	s_lshl_b32 s8, s9, 2
	s_lshl_b64 s[6:7], s[6:7], 24
	s_sext_i32_i16 s1, s1
	s_andn2_b32 s8, s8, 63
	v_and_b32_e32 v36, -4, v72
	s_ashr_i32 s9, s8, 31
	v_lshl_add_u64 v[34:35], v[66:67], 0, s[6:7]
	v_lshl_add_u32 v42, s1, 7, v36
	v_lshl_add_u64 v[34:35], s[8:9], 2, v[34:35]
	v_and_b32_e32 v36, 0xf0, v1
	v_mov_b32_e32 v37, 0
	v_ashrrev_i32_e32 v43, 31, v42
	v_lshl_add_u64 v[44:45], v[34:35], 0, v[36:37]
	v_lshlrev_b64 v[34:35], 13, v[42:43]
	v_lshl_add_u64 v[46:47], v[44:45], 0, v[34:35]
	v_or_b32_e32 v34, 1, v42
	v_ashrrev_i32_e32 v35, 31, v34
	v_lshlrev_b64 v[34:35], 13, v[34:35]
	v_lshl_add_u64 v[48:49], v[44:45], 0, v[34:35]
	global_load_dwordx4 v[34:37], v[46:47], off nt
	global_load_dwordx4 v[38:41], v[48:49], off nt
	v_or_b32_e32 v46, 2, v42
	v_ashrrev_i32_e32 v47, 31, v46
	v_or_b32_e32 v42, 3, v42
	v_lshlrev_b64 v[46:47], 13, v[46:47]
	v_ashrrev_i32_e32 v43, 31, v42
	v_lshl_add_u64 v[50:51], v[44:45], 0, v[46:47]
	v_lshlrev_b64 v[42:43], 13, v[42:43]
	v_lshl_add_u64 v[52:53], v[44:45], 0, v[42:43]
	global_load_dwordx4 v[42:45], v[50:51], off nt
	global_load_dwordx4 v[46:49], v[52:53], off nt
.LBB0_276:
	s_add_i32 s0, s0, s28
	s_cmpk_gt_i32 s0, 0x15ff
	s_cbranch_scc1 .LBB0_279
	s_ashr_i32 s1, s0, 31
	s_lshr_b32 s1, s1, 23
	s_add_i32 s1, s0, s1
	s_ashr_i32 s6, s1, 9
	s_and_b32 s1, s1, 0xfe00
	s_sub_i32 s8, s0, s1
	s_ashr_i32 s7, s6, 31
	s_lshl_b64 s[0:1], s[6:7], 24
	s_sext_i32_i16 s6, s8
	s_bfe_u32 s6, s6, 0x4001b
	s_add_i32 s6, s8, s6
	s_sext_i32_i16 s7, s6
	s_and_b32 s6, s6, 0xfff0
	s_sub_i32 s6, s8, s6
	s_sext_i32_i16 s8, s6
	s_lshl_b32 s6, s7, 2
	s_andn2_b32 s6, s6, 63
	v_and_b32_e32 v52, -4, v72
	s_ashr_i32 s7, s6, 31
	v_lshl_add_u64 v[50:51], v[66:67], 0, s[0:1]
	v_lshl_add_u32 v58, s8, 7, v52
	v_lshl_add_u64 v[50:51], s[6:7], 2, v[50:51]
	v_and_b32_e32 v52, 0xf0, v1
	v_mov_b32_e32 v53, 0
	v_ashrrev_i32_e32 v59, 31, v58
	v_lshl_add_u64 v[60:61], v[50:51], 0, v[52:53]
	v_lshlrev_b64 v[50:51], 13, v[58:59]
	v_lshl_add_u64 v[62:63], v[60:61], 0, v[50:51]
	v_or_b32_e32 v50, 1, v58
	v_ashrrev_i32_e32 v51, 31, v50
	v_lshlrev_b64 v[50:51], 13, v[50:51]
	v_lshl_add_u64 v[64:65], v[60:61], 0, v[50:51]
	global_load_dwordx4 v[50:53], v[62:63], off nt
	global_load_dwordx4 v[54:57], v[64:65], off nt
	v_or_b32_e32 v62, 2, v58
	v_ashrrev_i32_e32 v63, 31, v62
	v_or_b32_e32 v58, 3, v58
	v_lshlrev_b64 v[62:63], 13, v[62:63]
	v_ashrrev_i32_e32 v59, 31, v58
	v_lshl_add_u64 v[68:69], v[60:61], 0, v[62:63]
	v_lshlrev_b64 v[58:59], 13, v[58:59]
	v_lshl_add_u64 v[74:75], v[60:61], 0, v[58:59]
	global_load_dwordx4 v[58:61], v[68:69], off nt
	global_load_dwordx4 v[62:65], v[74:75], off nt
	s_andn2_b64 vcc, exec, s[2:3]
	s_cbranch_vccnz .LBB0_296
	s_branch .LBB0_280

; #define LAS __attribute__((address_space(3)))
; #define TB_LOAD(R_, t_) do { const int _t = (t_); if (_t < tot) { const int _b = _t / per, _r = _t % per; ttb_load(R_, src + (size_t)_b * K_ * N_, N_, (_r % kt) * 128, (_r / kt) * 64, C.tid); } } while (0)
; #define TB_STEP(R_, t_) do { const int _u = (t_); if (_u < tot) { LAS unsigned* tile = (LAS unsigned*)(C.lds + kbuf * 8192); ttb_put(R_, tile, C.tid); TB_LOAD(R_, _u + 4 * G); __syncthreads(); \
;         { const int _b = _u / per, _r = _u % per; ttb_finish(tile, dstb + (size_t)_b * K_ * (MAP_ == 2 ? 4096 : N_), K_, (_r % kt) * 128, (_r / kt) * 64, MAP_, C.tid); } kbuf ^= 1; } } while (0)
; __device__ __forceinline__ void ttb_put(const TReg& R, LAS unsigned* tile, int tid) {
;     const int kr = tid >> 4, nq = tid & 15;
; #pragma unroll
;     for (int c = 0; c < 4; ++c) { const int n = 4 * nq + c;
;         tile[n * 32 + (kr ^ (n & 31))] = pk4_fp8(R.v[0][c] * W_FP8_SCALE, R.v[1][c] * W_FP8_SCALE, R.v[2][c] * W_FP8_SCALE, R.v[3][c] * W_FP8_SCALE); } }
; __device__ __forceinline__ void ttb_finish(LAS const unsigned* tile, unsigned char* dst, int ldd, int k0, int n0, int map, int tid) {
;     const int n = tid >> 3, kq = tid & 7, m = n & 31, ns = n0 + n; int r = ns;
;     if (map == 2) { const int j = ns >> 1, par = ns & 1; r = 256 * (j >> 7) + 128 * par + (j & 127); }
;     const u32x4 g = *(LAS const u32x4*)(tile + n * 32 + 4 * (kq ^ (m >> 2)));
;     const unsigned a0 = (m & 1) ? g.y : g.x, a1 = (m & 1) ? g.x : g.y, a2 = (m & 1) ? g.w : g.z, a3 = (m & 1) ? g.z : g.w;
;     u32x4 w; w.x = (m & 2) ? a2 : a0; w.y = (m & 2) ? a3 : a1; w.z = (m & 2) ? a0 : a2; w.w = (m & 2) ? a1 : a3;
;     __builtin_nontemporal_store(w, (u32x4*)(dst + (size_t)r * ldd + k0 + 16 * kq));
; }
; template <int K_, int N_, int MAP_> __device__ __forceinline__ void tjob_b(const Ctx& C, int bid, int G, const float* src, unsigned char* dstb, int nbatch) {
;     constexpr int kt = K_ / 128, ntile = N_ / 64, per = kt * ntile; const int tot = per * nbatch;
;     TReg R0, R1, R2, R3; int kbuf = 0;
;     ...
;     TB_LOAD(R0, bid); TB_LOAD(R1, bid + G); TB_LOAD(R2, bid + 2 * G); TB_LOAD(R3, bid + 3 * G);
;     for (int t = bid; t < tot; t += 4 * G) { TB_STEP(R0, t); TB_STEP(R1, t + G); TB_STEP(R2, t + 2 * G); TB_STEP(R3, t + 3 * G); }
.LBB0_280:
	v_lshlrev_b32_e32 v1, 2, v70
	v_and_b32_e32 v68, 60, v1
	v_ashrrev_i32_e32 v71, 4, v70
	v_or_b32_e32 v73, 2, v68
	v_readlane_b32 s2, v254, 2
	v_or_b32_e32 v69, 1, v68
	v_bitop3_b32 v82, v73, v71, 30 bitop3:0x6c
	v_lshlrev_b32_e32 v74, 7, v73
	v_or_b32_e32 v73, 3, v68
	v_readlane_b32 s3, v254, 3
	s_add_u32 s0, s62, 0x2ed10000
	v_bitop3_b32 v80, v1, v71, 28 bitop3:0x6c
	v_bitop3_b32 v81, v69, v71, 29 bitop3:0x6c
	v_bitop3_b32 v83, v73, v71, 31 bitop3:0x6c
	v_and_b32_e32 v71, 7, v70
	s_mov_b32 s16, s2
	s_mul_i32 s2, s2, 7
	s_mul_i32 s3, s30, 7
	s_addc_u32 s1, s63, 0
	v_lshlrev_b32_e32 v75, 7, v73
	v_ashrrev_i32_e32 v76, 3, v70
	v_lshlrev_b32_e32 v73, 2, v71
	s_sub_i32 s14, s2, s3
	s_mul_i32 s2, s30, 6
	v_bitop3_b32 v84, v76, v73, 28 bitop3:0x6c
	v_and_b32_e32 v73, 8, v70
	s_sub_i32 s15, s29, s2
	s_mul_i32 s2, s16, 5
	s_mul_i32 s30, s30, 5
	v_cmp_eq_u32_e64 s[6:7], 0, v73
	v_and_b32_e32 v70, 16, v70
	v_mov_b32_e32 v73, 0
	s_sub_i32 s16, s2, s30
	v_readlane_b32 s2, v254, 0
	s_lshl_b32 s10, s28, 1
	s_mul_i32 s11, s28, 3
	s_lshl_b32 s12, s28, 2
	v_lshlrev_b32_e32 v1, 7, v68
	v_lshlrev_b32_e32 v69, 7, v69
	v_lshlrev_b32_e32 v77, 7, v76
	s_mov_b32 s13, 0
	v_cmp_eq_u32_e64 s[8:9], 0, v70
	v_lshlrev_b32_e32 v70, 4, v71
	v_mov_b32_e32 v71, v73
	v_and_b32_e32 v78, -4, v72
	s_mov_b32 s17, 0xc3e00000
	v_mov_b32_e32 v79, 0x43e00000
	v_lshlrev_b32_e32 v80, 2, v80
	v_lshlrev_b32_e32 v81, 2, v81
	v_lshlrev_b32_e32 v82, 2, v82
	v_lshlrev_b32_e32 v83, 2, v83
	v_lshlrev_b32_e32 v84, 2, v84
	s_mov_b32 s19, s2
	v_readlane_b32 s3, v254, 1
	s_waitcnt vmcnt(0)
	s_branch .LBB0_283

; #define LAS __attribute__((address_space(3)))
; #define TB_LOAD(R_, t_) do { const int _t = (t_); if (_t < tot) { const int _b = _t / per, _r = _t % per; ttb_load(R_, src + (size_t)_b * K_ * N_, N_, (_r % kt) * 128, (_r / kt) * 64, C.tid); } } while (0)
; #define TB_STEP(R_, t_) do { const int _u = (t_); if (_u < tot) { LAS unsigned* tile = (LAS unsigned*)(C.lds + kbuf * 8192); ttb_put(R_, tile, C.tid); TB_LOAD(R_, _u + 4 * G); __syncthreads(); \
;         { const int _b = _u / per, _r = _u % per; ttb_finish(tile, dstb + (size_t)_b * K_ * (MAP_ == 2 ? 4096 : N_), K_, (_r % kt) * 128, (_r / kt) * 64, MAP_, C.tid); } kbuf ^= 1; } } while (0)
; __device__ __forceinline__ void ttb_put(const TReg& R, LAS unsigned* tile, int tid) {
;     const int kr = tid >> 4, nq = tid & 15;
; #pragma unroll
;     for (int c = 0; c < 4; ++c) { const int n = 4 * nq + c;
;         tile[n * 32 + (kr ^ (n & 31))] = pk4_fp8(R.v[0][c] * W_FP8_SCALE, R.v[1][c] * W_FP8_SCALE, R.v[2][c] * W_FP8_SCALE, R.v[3][c] * W_FP8_SCALE); } }
; __device__ __forceinline__ void ttb_finish(LAS const unsigned* tile, unsigned char* dst, int ldd, int k0, int n0, int map, int tid) {
;     const int n = tid >> 3, kq = tid & 7, m = n & 31, ns = n0 + n; int r = ns;
;     if (map == 2) { const int j = ns >> 1, par = ns & 1; r = 256 * (j >> 7) + 128 * par + (j & 127); }
;     const u32x4 g = *(LAS const u32x4*)(tile + n * 32 + 4 * (kq ^ (m >> 2)));
;     const unsigned a0 = (m & 1) ? g.y : g.x, a1 = (m & 1) ? g.x : g.y, a2 = (m & 1) ? g.w : g.z, a3 = (m & 1) ? g.z : g.w;
;     u32x4 w; w.x = (m & 2) ? a2 : a0; w.y = (m & 2) ? a3 : a1; w.z = (m & 2) ? a0 : a2; w.w = (m & 2) ? a1 : a3;
;     __builtin_nontemporal_store(w, (u32x4*)(dst + (size_t)r * ldd + k0 + 16 * kq));
; }
; template <int K_, int N_, int MAP_> __device__ __forceinline__ void tjob_b(const Ctx& C, int bid, int G, const float* src, unsigned char* dstb, int nbatch) {
;     constexpr int kt = K_ / 128, ntile = N_ / 64, per = kt * ntile; const int tot = per * nbatch;
;     TReg R0, R1, R2, R3; int kbuf = 0;
;     ...
;     TB_LOAD(R0, bid); TB_LOAD(R1, bid + G); TB_LOAD(R2, bid + 2 * G); TB_LOAD(R3, bid + 3 * G);
;     for (int t = bid; t < tot; t += 4 * G) { TB_STEP(R0, t); TB_STEP(R1, t + G); TB_STEP(R2, t + 2 * G); TB_STEP(R3, t + 3 * G); }
.LBB0_283:
	s_waitcnt vmcnt(16) lgkmcnt(0)
	s_add_i32 s84, s19, s11
	s_cmp_lt_i32 s84, 0x1600
	s_cbranch_scc1 .Lcv_jt_0
	s_waitcnt vmcnt(0)
.Lcv_jt_0:
	v_mul_f32_e32 v72, 0x43800000, v2
	v_mul_f32_e32 v85, 0x43800000, v6
	v_med3_f32 v72, v72, s17, v79
	v_med3_f32 v85, v85, s17, v79
	v_cvt_pk_fp8_f32 v87, v72, v85
	v_mul_f32_e32 v86, 0x43800000, v10
	v_mul_f32_e32 v72, 0x43800000, v14
	v_med3_f32 v85, v86, s17, v79
	v_med3_f32 v72, v72, s17, v79
	v_cvt_pk_fp8_f32 v87, v85, v72 op_sel:[0,0,1]
	v_mul_f32_e32 v72, 0x43800000, v3
	v_mul_f32_e32 v85, 0x43800000, v7
	v_med3_f32 v72, v72, s17, v79
	v_med3_f32 v85, v85, s17, v79
	v_cvt_pk_fp8_f32 v88, v72, v85
	v_mul_f32_e32 v86, 0x43800000, v11
	v_mul_f32_e32 v72, 0x43800000, v15
	v_med3_f32 v85, v86, s17, v79
	v_med3_f32 v72, v72, s17, v79
	s_lshl_b32 s2, s13, 13
	v_cvt_pk_fp8_f32 v88, v85, v72 op_sel:[0,0,1]
	s_add_i32 s20, s2, 0
	v_add3_u32 v72, s20, v1, v80
	ds_write_b32 v72, v87
	v_add3_u32 v72, s20, v69, v81
	ds_write_b32 v72, v88
	v_mul_f32_e32 v72, 0x43800000, v4
	v_mul_f32_e32 v85, 0x43800000, v8
	v_med3_f32 v72, v72, s17, v79
	v_med3_f32 v85, v85, s17, v79
	v_cvt_pk_fp8_f32 v87, v72, v85
	v_mul_f32_e32 v86, 0x43800000, v12
	v_mul_f32_e32 v72, 0x43800000, v16
	v_med3_f32 v85, v86, s17, v79
	v_med3_f32 v72, v72, s17, v79
	v_cvt_pk_fp8_f32 v87, v85, v72 op_sel:[0,0,1]
	v_mul_f32_e32 v72, 0x43800000, v5
	v_mul_f32_e32 v85, 0x43800000, v9
	v_med3_f32 v72, v72, s17, v79
	v_med3_f32 v85, v85, s17, v79
	v_cvt_pk_fp8_f32 v88, v72, v85
	v_mul_f32_e32 v86, 0x43800000, v13
	v_mul_f32_e32 v72, 0x43800000, v17
	v_med3_f32 v85, v86, s17, v79
	v_med3_f32 v72, v72, s17, v79
	v_cvt_pk_fp8_f32 v88, v85, v72 op_sel:[0,0,1]
	s_add_i32 s18, s19, s12
	s_cmpk_gt_i32 s18, 0x15ff
	v_add3_u32 v72, s20, v74, v82
	s_cselect_b64 s[2:3], -1, 0
	ds_write_b32 v72, v87
	v_add3_u32 v72, s20, v75, v83
	s_and_b64 vcc, exec, s[2:3]
	ds_write_b32 v72, v88
	s_cbranch_vccnz .LBB0_285
	s_ashr_i32 s21, s18, 31
	s_lshr_b32 s21, s21, 23
	s_add_i32 s21, s18, s21
	s_ashr_i32 s22, s21, 9
	s_and_b32 s21, s21, 0xfe00
	s_ashr_i32 s23, s22, 31
	s_sub_i32 s21, s18, s21
	s_lshl_b64 s[22:23], s[22:23], 24
	v_lshl_add_u64 v[2:3], v[66:67], 0, s[22:23]
	s_sext_i32_i16 s22, s21
	s_bfe_u32 s22, s22, 0x4001b
	s_add_i32 s22, s21, s22
	s_sext_i32_i16 s23, s22
	s_and_b32 s22, s22, 0xfff0
	s_sub_i32 s21, s21, s22
	s_lshl_b32 s22, s23, 2
	s_sext_i32_i16 s21, s21
	s_andn2_b32 s22, s22, 63
	v_lshl_add_u32 v10, s21, 7, v78
	s_ashr_i32 s23, s22, 31
	v_lshl_add_u64 v[2:3], s[22:23], 2, v[2:3]
	v_lshlrev_b32_e32 v72, 2, v68
	v_ashrrev_i32_e32 v11, 31, v10
	v_lshl_add_u64 v[12:13], v[2:3], 0, v[72:73]
	v_lshlrev_b64 v[2:3], 13, v[10:11]
	v_lshl_add_u64 v[14:15], v[12:13], 0, v[2:3]
	v_or_b32_e32 v2, 1, v10
	v_ashrrev_i32_e32 v3, 31, v2
	v_lshlrev_b64 v[2:3], 13, v[2:3]
	v_lshl_add_u64 v[16:17], v[12:13], 0, v[2:3]
	global_load_dwordx4 v[2:5], v[14:15], off nt
	global_load_dwordx4 v[6:9], v[16:17], off nt
	v_or_b32_e32 v14, 2, v10
	v_ashrrev_i32_e32 v15, 31, v14
	v_or_b32_e32 v10, 3, v10
	v_lshlrev_b64 v[14:15], 13, v[14:15]
	v_ashrrev_i32_e32 v11, 31, v10
	v_lshl_add_u64 v[86:87], v[12:13], 0, v[14:15]
	v_lshlrev_b64 v[10:11], 13, v[10:11]
	v_lshl_add_u64 v[88:89], v[12:13], 0, v[10:11]
	global_load_dwordx4 v[10:13], v[86:87], off nt
	global_load_dwordx4 v[14:17], v[88:89], off nt
; #define LAS __attribute__((address_space(3)))
; #define TB_LOAD(R_, t_) do { const int _t = (t_); if (_t < tot) { const int _b = _t / per, _r = _t % per; ttb_load(R_, src + (size_t)_b * K_ * N_, N_, (_r % kt) * 128, (_r / kt) * 64, C.tid); } } while (0)
; #define TB_STEP(R_, t_) do { const int _u = (t_); if (_u < tot) { LAS unsigned* tile = (LAS unsigned*)(C.lds + kbuf * 8192); ttb_put(R_, tile, C.tid); TB_LOAD(R_, _u + 4 * G); __syncthreads(); \
;         { const int _b = _u / per, _r = _u % per; ttb_finish(tile, dstb + (size_t)_b * K_ * (MAP_ == 2 ? 4096 : N_), K_, (_r % kt) * 128, (_r / kt) * 64, MAP_, C.tid); } kbuf ^= 1; } } while (0)
; __device__ __forceinline__ void ttb_put(const TReg& R, LAS unsigned* tile, int tid) {
;     const int kr = tid >> 4, nq = tid & 15;
; #pragma unroll
;     for (int c = 0; c < 4; ++c) { const int n = 4 * nq + c;
;         tile[n * 32 + (kr ^ (n & 31))] = pk4_fp8(R.v[0][c] * W_FP8_SCALE, R.v[1][c] * W_FP8_SCALE, R.v[2][c] * W_FP8_SCALE, R.v[3][c] * W_FP8_SCALE); } }
; __device__ __forceinline__ void ttb_finish(LAS const unsigned* tile, unsigned char* dst, int ldd, int k0, int n0, int map, int tid) {
;     const int n = tid >> 3, kq = tid & 7, m = n & 31, ns = n0 + n; int r = ns;
;     if (map == 2) { const int j = ns >> 1, par = ns & 1; r = 256 * (j >> 7) + 128 * par + (j & 127); }
;     const u32x4 g = *(LAS const u32x4*)(tile + n * 32 + 4 * (kq ^ (m >> 2)));
;     const unsigned a0 = (m & 1) ? g.y : g.x, a1 = (m & 1) ? g.x : g.y, a2 = (m & 1) ? g.w : g.z, a3 = (m & 1) ? g.z : g.w;
;     u32x4 w; w.x = (m & 2) ? a2 : a0; w.y = (m & 2) ? a3 : a1; w.z = (m & 2) ? a0 : a2; w.w = (m & 2) ? a1 : a3;
;     __builtin_nontemporal_store(w, (u32x4*)(dst + (size_t)r * ldd + k0 + 16 * kq));
; }
; template <int K_, int N_, int MAP_> __device__ __forceinline__ void tjob_b(const Ctx& C, int bid, int G, const float* src, unsigned char* dstb, int nbatch) {
;     constexpr int kt = K_ / 128, ntile = N_ / 64, per = kt * ntile; const int tot = per * nbatch;
;     TReg R0, R1, R2, R3; int kbuf = 0;
;     ...
;     TB_LOAD(R0, bid); TB_LOAD(R1, bid + G); TB_LOAD(R2, bid + 2 * G); TB_LOAD(R3, bid + 3 * G);
;     for (int t = bid; t < tot; t += 4 * G) { TB_STEP(R0, t); TB_STEP(R1, t + G); TB_STEP(R2, t + 2 * G); TB_STEP(R3, t + 3 * G); }
.LBB0_285:
	s_ashr_i32 s21, s19, 31
	s_lshr_b32 s21, s21, 23
	s_add_i32 s21, s19, s21
	s_ashr_i32 s22, s21, 9
	s_and_b32 s21, s21, 0xfe00
	s_ashr_i32 s23, s22, 31
	s_sub_i32 s21, s19, s21
	s_lshl_b64 s[22:23], s[22:23], 22
	s_add_u32 s22, s0, s22
	s_sext_i32_i16 s24, s21
	s_addc_u32 s23, s1, s23
	s_bfe_u32 s24, s24, 0x4001b
	s_add_i32 s24, s21, s24
	v_add3_u32 v72, s20, v77, v84
	s_waitcnt lgkmcnt(0)
	s_barrier
	s_sext_i32_i16 s25, s24
	s_and_b32 s24, s24, 0xfff0
	ds_read_b128 v[86:89], v72
	s_sub_i32 s21, s21, s24
	s_sext_i32_i16 s21, s21
	s_lshl_b32 s20, s21, 7
	s_lshl_b32 s21, s25, 2
	s_andn2_b32 s21, s21, 63
	v_add_u32_e32 v90, s21, v76
	s_waitcnt lgkmcnt(0)
	v_cndmask_b32_e64 v72, v87, v86, s[6:7]
	v_cndmask_b32_e64 v91, v89, v88, s[6:7]
	v_cndmask_b32_e64 v85, v86, v87, s[6:7]
	v_cndmask_b32_e64 v89, v88, v89, s[6:7]
	v_cndmask_b32_e64 v86, v91, v72, s[8:9]
	v_cndmask_b32_e64 v88, v72, v91, s[8:9]
	v_ashrrev_i32_e32 v91, 31, v90
	v_lshlrev_b64 v[90:91], 11, v[90:91]
	v_lshl_add_u64 v[90:91], s[22:23], 0, v[90:91]
	s_ashr_i32 s21, s20, 31
	v_lshl_add_u64 v[90:91], v[90:91], 0, s[20:21]
	s_xor_b32 s21, s13, 1
	s_add_i32 s20, s28, s19
	v_cndmask_b32_e64 v87, v89, v85, s[8:9]
	v_cndmask_b32_e64 v89, v85, v89, s[8:9]
	v_lshl_add_u64 v[90:91], v[90:91], 0, v[70:71]
	s_cmpk_gt_i32 s20, 0x15ff
	global_store_dwordx4 v[90:91], v[86:89], off nt
	s_cbranch_scc1 .LBB0_289
	s_waitcnt vmcnt(16)
	s_add_i32 s84, s20, s11
	s_cmp_lt_i32 s84, 0x1600
	s_cbranch_scc1 .Lcv_jt_1
	s_waitcnt vmcnt(0)
.Lcv_jt_1:
	v_mul_f32_e32 v72, 0x43800000, v18
	v_mul_f32_e32 v85, 0x43800000, v22
	v_med3_f32 v72, v72, s17, v79
	v_med3_f32 v85, v85, s17, v79
	v_cvt_pk_fp8_f32 v87, v72, v85
	v_mul_f32_e32 v86, 0x43800000, v26
	v_mul_f32_e32 v72, 0x43800000, v30
	v_med3_f32 v85, v86, s17, v79
	v_med3_f32 v72, v72, s17, v79
	v_cvt_pk_fp8_f32 v87, v85, v72 op_sel:[0,0,1]
	s_lshl_b32 s21, s21, 13
	s_add_i32 s21, s21, 0
	v_add3_u32 v72, s21, v1, v80
	ds_write_b32 v72, v87
	v_mul_f32_e32 v72, 0x43800000, v19
	v_mul_f32_e32 v85, 0x43800000, v23
	v_med3_f32 v72, v72, s17, v79
	v_med3_f32 v85, v85, s17, v79
	v_cvt_pk_fp8_f32 v87, v72, v85
	v_mul_f32_e32 v86, 0x43800000, v27
	v_mul_f32_e32 v72, 0x43800000, v31
	v_med3_f32 v85, v86, s17, v79
	v_med3_f32 v72, v72, s17, v79
	v_cvt_pk_fp8_f32 v87, v85, v72 op_sel:[0,0,1]
	v_mul_f32_e32 v72, 0x43800000, v20
	v_mul_f32_e32 v85, 0x43800000, v24
	v_med3_f32 v72, v72, s17, v79
	v_med3_f32 v85, v85, s17, v79
	v_cvt_pk_fp8_f32 v88, v72, v85
	v_mul_f32_e32 v86, 0x43800000, v28
	v_mul_f32_e32 v72, 0x43800000, v32
	v_med3_f32 v85, v86, s17, v79
	v_med3_f32 v72, v72, s17, v79
	v_cvt_pk_fp8_f32 v88, v85, v72 op_sel:[0,0,1]
	v_add3_u32 v72, s21, v69, v81
	ds_write_b32 v72, v87
	v_add3_u32 v72, s21, v74, v82
	ds_write_b32 v72, v88
	v_mul_f32_e32 v72, 0x43800000, v21
	v_mul_f32_e32 v85, 0x43800000, v25
	v_med3_f32 v72, v72, s17, v79
	v_med3_f32 v85, v85, s17, v79
	v_cvt_pk_fp8_f32 v87, v72, v85
	v_mul_f32_e32 v86, 0x43800000, v29
	v_mul_f32_e32 v72, 0x43800000, v33
	v_med3_f32 v85, v86, s17, v79
	v_med3_f32 v72, v72, s17, v79
	v_cvt_pk_fp8_f32 v87, v85, v72 op_sel:[0,0,1]
	s_add_i32 s22, s16, s19
	v_add3_u32 v72, s21, v75, v83
	s_cmpk_gt_i32 s22, 0x15ff
	ds_write_b32 v72, v87
	s_cbranch_scc1 .LBB0_288
	s_ashr_i32 s23, s22, 31
	s_lshr_b32 s23, s23, 23
	s_add_i32 s23, s22, s23
	s_ashr_i32 s24, s23, 9
	s_and_b32 s23, s23, 0xfe00
	s_ashr_i32 s25, s24, 31
	s_sub_i32 s26, s22, s23
	s_lshl_b64 s[22:23], s[24:25], 24
	v_lshl_add_u64 v[18:19], v[66:67], 0, s[22:23]
	s_sext_i32_i16 s22, s26
	s_bfe_u32 s22, s22, 0x4001b
	s_add_i32 s22, s26, s22
	s_sext_i32_i16 s23, s22
	s_and_b32 s22, s22, 0xfff0
	s_sub_i32 s22, s26, s22
	s_sext_i32_i16 s24, s22
	s_lshl_b32 s22, s23, 2
	s_andn2_b32 s22, s22, 63
	v_lshl_add_u32 v26, s24, 7, v78
	s_ashr_i32 s23, s22, 31
	v_lshl_add_u64 v[18:19], s[22:23], 2, v[18:19]
	v_lshlrev_b32_e32 v72, 2, v68
	v_ashrrev_i32_e32 v27, 31, v26
	v_lshl_add_u64 v[28:29], v[18:19], 0, v[72:73]
	v_lshlrev_b64 v[18:19], 13, v[26:27]
	v_lshl_add_u64 v[30:31], v[28:29], 0, v[18:19]
	v_or_b32_e32 v18, 1, v26
	v_ashrrev_i32_e32 v19, 31, v18
	v_lshlrev_b64 v[18:19], 13, v[18:19]
	v_lshl_add_u64 v[32:33], v[28:29], 0, v[18:19]
	global_load_dwordx4 v[18:21], v[30:31], off nt
	global_load_dwordx4 v[22:25], v[32:33], off nt
	v_or_b32_e32 v30, 2, v26
	v_ashrrev_i32_e32 v31, 31, v30
	v_or_b32_e32 v26, 3, v26
	v_lshlrev_b64 v[30:31], 13, v[30:31]
	v_ashrrev_i32_e32 v27, 31, v26
	v_lshl_add_u64 v[86:87], v[28:29], 0, v[30:31]
	v_lshlrev_b64 v[26:27], 13, v[26:27]
	v_lshl_add_u64 v[88:89], v[28:29], 0, v[26:27]
	global_load_dwordx4 v[26:29], v[86:87], off nt
	global_load_dwordx4 v[30:33], v[88:89], off nt

; #define LAS __attribute__((address_space(3)))
; #define TB_LOAD(R_, t_) do { const int _t = (t_); if (_t < tot) { const int _b = _t / per, _r = _t % per; ttb_load(R_, src + (size_t)_b * K_ * N_, N_, (_r % kt) * 128, (_r / kt) * 64, C.tid); } } while (0)
; #define TB_STEP(R_, t_) do { const int _u = (t_); if (_u < tot) { LAS unsigned* tile = (LAS unsigned*)(C.lds + kbuf * 8192); ttb_put(R_, tile, C.tid); TB_LOAD(R_, _u + 4 * G); __syncthreads(); \
;         { const int _b = _u / per, _r = _u % per; ttb_finish(tile, dstb + (size_t)_b * K_ * (MAP_ == 2 ? 4096 : N_), K_, (_r % kt) * 128, (_r / kt) * 64, MAP_, C.tid); } kbuf ^= 1; } } while (0)
; __device__ __forceinline__ void ttb_put(const TReg& R, LAS unsigned* tile, int tid) {
;     const int kr = tid >> 4, nq = tid & 15;
; #pragma unroll
;     for (int c = 0; c < 4; ++c) { const int n = 4 * nq + c;
;         tile[n * 32 + (kr ^ (n & 31))] = pk4_fp8(R.v[0][c] * W_FP8_SCALE, R.v[1][c] * W_FP8_SCALE, R.v[2][c] * W_FP8_SCALE, R.v[3][c] * W_FP8_SCALE); } }
; __device__ __forceinline__ void ttb_finish(LAS const unsigned* tile, unsigned char* dst, int ldd, int k0, int n0, int map, int tid) {
;     const int n = tid >> 3, kq = tid & 7, m = n & 31, ns = n0 + n; int r = ns;
;     if (map == 2) { const int j = ns >> 1, par = ns & 1; r = 256 * (j >> 7) + 128 * par + (j & 127); }
;     const u32x4 g = *(LAS const u32x4*)(tile + n * 32 + 4 * (kq ^ (m >> 2)));
;     const unsigned a0 = (m & 1) ? g.y : g.x, a1 = (m & 1) ? g.x : g.y, a2 = (m & 1) ? g.w : g.z, a3 = (m & 1) ? g.z : g.w;
;     u32x4 w; w.x = (m & 2) ? a2 : a0; w.y = (m & 2) ? a3 : a1; w.z = (m & 2) ? a0 : a2; w.w = (m & 2) ? a1 : a3;
;     __builtin_nontemporal_store(w, (u32x4*)(dst + (size_t)r * ldd + k0 + 16 * kq));
; }
; template <int K_, int N_, int MAP_> __device__ __forceinline__ void tjob_b(const Ctx& C, int bid, int G, const float* src, unsigned char* dstb, int nbatch) {
;     constexpr int kt = K_ / 128, ntile = N_ / 64, per = kt * ntile; const int tot = per * nbatch;
;     TReg R0, R1, R2, R3; int kbuf = 0;
;     ...
;     TB_LOAD(R0, bid); TB_LOAD(R1, bid + G); TB_LOAD(R2, bid + 2 * G); TB_LOAD(R3, bid + 3 * G);
;     for (int t = bid; t < tot; t += 4 * G) { TB_STEP(R0, t); TB_STEP(R1, t + G); TB_STEP(R2, t + 2 * G); TB_STEP(R3, t + 3 * G); }
.LBB0_290:
	s_waitcnt vmcnt(16)
	s_add_i32 s84, s20, s11
	s_cmp_lt_i32 s84, 0x1600
	s_cbranch_scc1 .Lcv_jt_2
	s_waitcnt vmcnt(0)
.Lcv_jt_2:
	v_mul_f32_e32 v72, 0x43800000, v34
	v_mul_f32_e32 v85, 0x43800000, v38
	v_med3_f32 v72, v72, s17, v79
	v_med3_f32 v85, v85, s17, v79
	v_cvt_pk_fp8_f32 v87, v72, v85
	v_mul_f32_e32 v86, 0x43800000, v42
	v_mul_f32_e32 v72, 0x43800000, v46
	v_med3_f32 v85, v86, s17, v79
	v_med3_f32 v72, v72, s17, v79
	v_cvt_pk_fp8_f32 v87, v85, v72 op_sel:[0,0,1]
	s_lshl_b32 s21, s13, 13
	s_add_i32 s21, s21, 0
	v_add3_u32 v72, s21, v1, v80
	ds_write_b32 v72, v87
	v_mul_f32_e32 v72, 0x43800000, v35
	v_mul_f32_e32 v85, 0x43800000, v39
	v_med3_f32 v72, v72, s17, v79
	v_med3_f32 v85, v85, s17, v79
	v_cvt_pk_fp8_f32 v87, v72, v85
	v_mul_f32_e32 v86, 0x43800000, v43
	v_mul_f32_e32 v72, 0x43800000, v47
	v_med3_f32 v85, v86, s17, v79
	v_med3_f32 v72, v72, s17, v79
	v_cvt_pk_fp8_f32 v87, v85, v72 op_sel:[0,0,1]
	v_mul_f32_e32 v72, 0x43800000, v36
	v_mul_f32_e32 v85, 0x43800000, v40
	v_med3_f32 v72, v72, s17, v79
	v_med3_f32 v85, v85, s17, v79
	v_cvt_pk_fp8_f32 v88, v72, v85
	v_mul_f32_e32 v86, 0x43800000, v44
	v_mul_f32_e32 v72, 0x43800000, v48
	v_med3_f32 v85, v86, s17, v79
	v_med3_f32 v72, v72, s17, v79
	v_cvt_pk_fp8_f32 v88, v85, v72 op_sel:[0,0,1]
	v_add3_u32 v72, s21, v69, v81
	ds_write_b32 v72, v87
	v_add3_u32 v72, s21, v74, v82
	ds_write_b32 v72, v88
	v_mul_f32_e32 v72, 0x43800000, v37
	v_mul_f32_e32 v85, 0x43800000, v41
	v_med3_f32 v72, v72, s17, v79
	v_med3_f32 v85, v85, s17, v79
	v_cvt_pk_fp8_f32 v87, v72, v85
	v_mul_f32_e32 v86, 0x43800000, v45
	v_mul_f32_e32 v72, 0x43800000, v49
	v_med3_f32 v85, v86, s17, v79
	v_med3_f32 v72, v72, s17, v79
	v_cvt_pk_fp8_f32 v87, v85, v72 op_sel:[0,0,1]
	s_add_i32 s22, s15, s19
	v_add3_u32 v72, s21, v75, v83
	s_cmpk_gt_i32 s22, 0x15ff
	ds_write_b32 v72, v87
	s_cbranch_scc1 .LBB0_292
	s_ashr_i32 s23, s22, 31
	s_lshr_b32 s23, s23, 23
	s_add_i32 s23, s22, s23
	s_ashr_i32 s24, s23, 9
	s_and_b32 s23, s23, 0xfe00
	s_ashr_i32 s25, s24, 31
	s_sub_i32 s26, s22, s23
	s_lshl_b64 s[22:23], s[24:25], 24
	v_lshl_add_u64 v[34:35], v[66:67], 0, s[22:23]
	s_sext_i32_i16 s22, s26
	s_bfe_u32 s22, s22, 0x4001b
	s_add_i32 s22, s26, s22
	s_sext_i32_i16 s23, s22
	s_and_b32 s22, s22, 0xfff0
	s_sub_i32 s22, s26, s22
	s_sext_i32_i16 s24, s22
	s_lshl_b32 s22, s23, 2
	s_andn2_b32 s22, s22, 63
	v_lshl_add_u32 v42, s24, 7, v78
	s_ashr_i32 s23, s22, 31
	v_lshl_add_u64 v[34:35], s[22:23], 2, v[34:35]
	v_lshlrev_b32_e32 v72, 2, v68
	v_ashrrev_i32_e32 v43, 31, v42
	v_lshl_add_u64 v[44:45], v[34:35], 0, v[72:73]
	v_lshlrev_b64 v[34:35], 13, v[42:43]
	v_lshl_add_u64 v[46:47], v[44:45], 0, v[34:35]
	v_or_b32_e32 v34, 1, v42
	v_ashrrev_i32_e32 v35, 31, v34
	v_lshlrev_b64 v[34:35], 13, v[34:35]
	v_lshl_add_u64 v[48:49], v[44:45], 0, v[34:35]
	global_load_dwordx4 v[34:37], v[46:47], off nt
	global_load_dwordx4 v[38:41], v[48:49], off nt
	v_or_b32_e32 v46, 2, v42
	v_ashrrev_i32_e32 v47, 31, v46
	v_or_b32_e32 v42, 3, v42
	v_lshlrev_b64 v[46:47], 13, v[46:47]
	v_ashrrev_i32_e32 v43, 31, v42
	v_lshl_add_u64 v[86:87], v[44:45], 0, v[46:47]
	v_lshlrev_b64 v[42:43], 13, v[42:43]
	v_lshl_add_u64 v[88:89], v[44:45], 0, v[42:43]
	global_load_dwordx4 v[42:45], v[86:87], off nt
	global_load_dwordx4 v[46:49], v[88:89], off nt

; #define LAS __attribute__((address_space(3)))
; #define TB_LOAD(R_, t_) do { const int _t = (t_); if (_t < tot) { const int _b = _t / per, _r = _t % per; ttb_load(R_, src + (size_t)_b * K_ * N_, N_, (_r % kt) * 128, (_r / kt) * 64, C.tid); } } while (0)
; #define TB_STEP(R_, t_) do { const int _u = (t_); if (_u < tot) { LAS unsigned* tile = (LAS unsigned*)(C.lds + kbuf * 8192); ttb_put(R_, tile, C.tid); TB_LOAD(R_, _u + 4 * G); __syncthreads(); \
;         { const int _b = _u / per, _r = _u % per; ttb_finish(tile, dstb + (size_t)_b * K_ * (MAP_ == 2 ? 4096 : N_), K_, (_r % kt) * 128, (_r / kt) * 64, MAP_, C.tid); } kbuf ^= 1; } } while (0)
; __device__ __forceinline__ void ttb_put(const TReg& R, LAS unsigned* tile, int tid) {
;     const int kr = tid >> 4, nq = tid & 15;
; #pragma unroll
;     for (int c = 0; c < 4; ++c) { const int n = 4 * nq + c;
;         tile[n * 32 + (kr ^ (n & 31))] = pk4_fp8(R.v[0][c] * W_FP8_SCALE, R.v[1][c] * W_FP8_SCALE, R.v[2][c] * W_FP8_SCALE, R.v[3][c] * W_FP8_SCALE); } }
; __device__ __forceinline__ void ttb_finish(LAS const unsigned* tile, unsigned char* dst, int ldd, int k0, int n0, int map, int tid) {
;     const int n = tid >> 3, kq = tid & 7, m = n & 31, ns = n0 + n; int r = ns;
;     if (map == 2) { const int j = ns >> 1, par = ns & 1; r = 256 * (j >> 7) + 128 * par + (j & 127); }
;     const u32x4 g = *(LAS const u32x4*)(tile + n * 32 + 4 * (kq ^ (m >> 2)));
;     const unsigned a0 = (m & 1) ? g.y : g.x, a1 = (m & 1) ? g.x : g.y, a2 = (m & 1) ? g.w : g.z, a3 = (m & 1) ? g.z : g.w;
;     u32x4 w; w.x = (m & 2) ? a2 : a0; w.y = (m & 2) ? a3 : a1; w.z = (m & 2) ? a0 : a2; w.w = (m & 2) ? a1 : a3;
;     __builtin_nontemporal_store(w, (u32x4*)(dst + (size_t)r * ldd + k0 + 16 * kq));
; }
; template <int K_, int N_, int MAP_> __device__ __forceinline__ void tjob_b(const Ctx& C, int bid, int G, const float* src, unsigned char* dstb, int nbatch) {
;     constexpr int kt = K_ / 128, ntile = N_ / 64, per = kt * ntile; const int tot = per * nbatch;
;     TReg R0, R1, R2, R3; int kbuf = 0;
;     ...
;     TB_LOAD(R0, bid); TB_LOAD(R1, bid + G); TB_LOAD(R2, bid + 2 * G); TB_LOAD(R3, bid + 3 * G);
;     for (int t = bid; t < tot; t += 4 * G) { TB_STEP(R0, t); TB_STEP(R1, t + G); TB_STEP(R2, t + 2 * G); TB_STEP(R3, t + 3 * G); }
.LBB0_293:
	s_add_i32 s20, s11, s19
	s_cmpk_gt_i32 s20, 0x15ff
	s_cbranch_scc1 .LBB0_282
	s_waitcnt vmcnt(16)
	s_add_i32 s84, s20, s11
	s_cmp_lt_i32 s84, 0x1600
	s_cbranch_scc1 .Lcv_jt_3
	s_waitcnt vmcnt(0)
.Lcv_jt_3:
	v_mul_f32_e32 v72, 0x43800000, v50
	v_mul_f32_e32 v85, 0x43800000, v54
	v_med3_f32 v72, v72, s17, v79
	v_med3_f32 v85, v85, s17, v79
	v_cvt_pk_fp8_f32 v87, v72, v85
	v_mul_f32_e32 v86, 0x43800000, v58
	v_mul_f32_e32 v72, 0x43800000, v62
	v_med3_f32 v85, v86, s17, v79
	v_med3_f32 v72, v72, s17, v79
	v_cvt_pk_fp8_f32 v87, v85, v72 op_sel:[0,0,1]
	s_lshl_b32 s21, s13, 13
	s_add_i32 s21, s21, 0
	v_add3_u32 v72, s21, v1, v80
	ds_write_b32 v72, v87
	v_mul_f32_e32 v72, 0x43800000, v51
	v_mul_f32_e32 v85, 0x43800000, v55
	v_med3_f32 v72, v72, s17, v79
	v_med3_f32 v85, v85, s17, v79
	v_cvt_pk_fp8_f32 v87, v72, v85
	v_mul_f32_e32 v86, 0x43800000, v59
	v_mul_f32_e32 v72, 0x43800000, v63
	v_med3_f32 v85, v86, s17, v79
	v_med3_f32 v72, v72, s17, v79
	v_cvt_pk_fp8_f32 v87, v85, v72 op_sel:[0,0,1]
	v_mul_f32_e32 v72, 0x43800000, v52
	v_mul_f32_e32 v85, 0x43800000, v56
	v_med3_f32 v72, v72, s17, v79
	v_med3_f32 v85, v85, s17, v79
	v_cvt_pk_fp8_f32 v88, v72, v85
	v_mul_f32_e32 v86, 0x43800000, v60
	v_mul_f32_e32 v72, 0x43800000, v64
	v_med3_f32 v85, v86, s17, v79
	v_med3_f32 v72, v72, s17, v79
	v_cvt_pk_fp8_f32 v88, v85, v72 op_sel:[0,0,1]
	v_add3_u32 v72, s21, v69, v81
	ds_write_b32 v72, v87
	v_add3_u32 v72, s21, v74, v82
	ds_write_b32 v72, v88
	v_mul_f32_e32 v72, 0x43800000, v53
	v_mul_f32_e32 v85, 0x43800000, v57
	v_med3_f32 v72, v72, s17, v79
	v_med3_f32 v85, v85, s17, v79
	v_cvt_pk_fp8_f32 v87, v72, v85
	v_mul_f32_e32 v86, 0x43800000, v61
	v_mul_f32_e32 v72, 0x43800000, v65
	v_med3_f32 v85, v86, s17, v79
	v_med3_f32 v72, v72, s17, v79
	v_cvt_pk_fp8_f32 v87, v85, v72 op_sel:[0,0,1]
	s_add_i32 s19, s14, s19
	v_add3_u32 v72, s21, v75, v83
	s_cmpk_gt_i32 s19, 0x15ff
	ds_write_b32 v72, v87
	s_cbranch_scc1 .LBB0_281
	s_ashr_i32 s22, s19, 31
	s_lshr_b32 s22, s22, 23
	s_add_i32 s23, s19, s22
	s_ashr_i32 s22, s23, 9
	s_and_b32 s23, s23, 0xfe00
	s_sub_i32 s19, s19, s23
	s_ashr_i32 s23, s22, 31
	s_lshl_b64 s[22:23], s[22:23], 24
	v_lshl_add_u64 v[50:51], v[66:67], 0, s[22:23]
	s_sext_i32_i16 s22, s19
	s_bfe_u32 s22, s22, 0x4001b
	s_add_i32 s22, s19, s22
	s_sext_i32_i16 s23, s22
	s_and_b32 s22, s22, 0xfff0
	s_sub_i32 s19, s19, s22
	s_lshl_b32 s22, s23, 2
	s_sext_i32_i16 s19, s19
	s_andn2_b32 s22, s22, 63
	v_lshl_add_u32 v58, s19, 7, v78
	s_ashr_i32 s23, s22, 31
	v_lshl_add_u64 v[50:51], s[22:23], 2, v[50:51]
	v_lshlrev_b32_e32 v72, 2, v68
	v_ashrrev_i32_e32 v59, 31, v58
	v_lshl_add_u64 v[60:61], v[50:51], 0, v[72:73]
	v_lshlrev_b64 v[50:51], 13, v[58:59]
	v_lshl_add_u64 v[62:63], v[60:61], 0, v[50:51]
	v_or_b32_e32 v50, 1, v58
	v_ashrrev_i32_e32 v51, 31, v50
	v_lshlrev_b64 v[50:51], 13, v[50:51]
	v_lshl_add_u64 v[64:65], v[60:61], 0, v[50:51]
	global_load_dwordx4 v[50:53], v[62:63], off nt
	global_load_dwordx4 v[54:57], v[64:65], off nt
	v_or_b32_e32 v62, 2, v58
	v_ashrrev_i32_e32 v63, 31, v62
	v_or_b32_e32 v58, 3, v58
	v_lshlrev_b64 v[62:63], 13, v[62:63]
	v_ashrrev_i32_e32 v59, 31, v58
	v_lshl_add_u64 v[86:87], v[60:61], 0, v[62:63]
	v_lshlrev_b64 v[58:59], 13, v[58:59]
	v_lshl_add_u64 v[88:89], v[60:61], 0, v[58:59]
	global_load_dwordx4 v[58:61], v[86:87], off nt
	global_load_dwordx4 v[62:65], v[88:89], off nt
	s_branch .LBB0_281
